# W2 with the mid-block s_setprio 0/1 flip pair removed (32 back-to-back MFMAs per compute segment)
# baseline (speedup 1.0000x reference)
.LBB0_310:
	s_ashr_i32 s91, s90, 31
	s_lshl_b64 s[4:5], s[90:91], 20
	s_add_u32 s62, s66, s4
	s_addc_u32 s63, s67, s5
	s_and_b64 s[4:5], s[36:37], exec
	s_cselect_b32 s4, s63, s25
	s_cselect_b32 s5, s62, s24
	s_ashr_i32 s89, s88, 31
	s_lshl_b64 s[20:21], s[88:89], 20
	s_add_u32 s20, s72, s20
	s_addc_u32 s21, s73, s21
	s_and_b64 s[30:31], s[36:37], exec
	s_cselect_b32 s8, s21, s1
	s_cselect_b32 s13, s20, s0
	s_add_u32 s17, s0, 0x10000
	s_addc_u32 s19, s1, 0
	s_add_u32 s0, s24, 0x80080
	s_addc_u32 s1, s25, 0
	s_mov_b32 s28, -2
	v_add_u32_e32 v100, s3, v190
	v_add_u32_e32 v156, s75, v190
	ds_read_b128 v[40:43], v100
	ds_read_b128 v[60:63], v100 offset:1024
	ds_read_b128 v[80:83], v100 offset:2048
	ds_read_b128 v[100:103], v100 offset:3072
	ds_read_b128 v[120:123], v156
	ds_read_b128 v[140:143], v156 offset:1024
	ds_read_b128 v[152:155], v156 offset:2048
	ds_read_b128 v[156:159], v156 offset:3072
	s_add_u32 s24, s0, 0xfff80080
	s_addc_u32 s25, s1, -1
	s_cmp_eq_u32 s28, 28
	s_cselect_b32 s39, s4, s25
	s_cselect_b32 s38, s5, s24
	s_cselect_b32 s25, s8, s19
	s_cselect_b32 s24, s13, s17
	v_lshl_add_u64 v[188:189], s[0:1], 0, v[168:169]
	s_add_i32 m0, s78, 0xc000
	ds_read_b128 v[172:175], v191
	ds_read_b128 v[176:179], v191 offset:1024
	ds_read_b128 v[180:183], v191 offset:2048
	ds_read_b128 v[184:187], v191 offset:3072
	ds_read_b128 v[192:195], v191 offset:4096
	ds_read_b128 v[196:199], v191 offset:5120
	ds_read_b128 v[200:203], v191 offset:6144
	ds_read_b128 v[204:207], v191 offset:7168
	global_load_lds_dwordx4 v[188:189], off
	v_lshl_add_u64 v[188:189], s[0:1], 0, v[170:171]
	s_add_i32 m0, s78, 0xe000
	s_nop 0
	global_load_lds_dwordx4 v[188:189], off
	s_waitcnt vmcnt(8)
	s_waitcnt lgkmcnt(0)
	s_setprio 1
	s_barrier
	v_mfma_f32_16x16x32_bf16 v[148:151], v[40:43], v[172:175], 0
	v_mfma_f32_16x16x32_bf16 v[144:147], v[80:83], v[172:175], 0
	v_mfma_f32_16x16x32_bf16 v[128:131], v[40:43], v[180:183], 0
	v_mfma_f32_16x16x32_bf16 v[124:127], v[80:83], v[180:183], 0
	v_mfma_f32_16x16x32_bf16 v[108:111], v[40:43], v[192:195], 0
	v_mfma_f32_16x16x32_bf16 v[104:107], v[80:83], v[192:195], 0
	v_mfma_f32_16x16x32_bf16 v[88:91], v[40:43], v[200:203], 0
	v_mfma_f32_16x16x32_bf16 v[84:87], v[80:83], v[200:203], 0
	v_mfma_f32_16x16x32_bf16 v[148:151], v[60:63], v[176:179], v[148:151]
	v_mfma_f32_16x16x32_bf16 v[144:147], v[100:103], v[176:179], v[144:147]
	v_mfma_f32_16x16x32_bf16 v[128:131], v[60:63], v[184:187], v[128:131]
	v_mfma_f32_16x16x32_bf16 v[124:127], v[100:103], v[184:187], v[124:127]
	v_mfma_f32_16x16x32_bf16 v[108:111], v[60:63], v[196:199], v[108:111]
	v_mfma_f32_16x16x32_bf16 v[104:107], v[100:103], v[196:199], v[104:107]
	v_mfma_f32_16x16x32_bf16 v[88:91], v[60:63], v[204:207], v[88:91]
	v_mfma_f32_16x16x32_bf16 v[84:87], v[100:103], v[204:207], v[84:87]
	v_mfma_f32_16x16x32_bf16 v[136:139], v[120:123], v[172:175], 0
	v_mfma_f32_16x16x32_bf16 v[132:135], v[152:155], v[172:175], 0
	v_mfma_f32_16x16x32_bf16 v[116:119], v[120:123], v[180:183], 0
	v_mfma_f32_16x16x32_bf16 v[112:115], v[152:155], v[180:183], 0
	v_mfma_f32_16x16x32_bf16 v[96:99], v[120:123], v[192:195], 0
	v_mfma_f32_16x16x32_bf16 v[92:95], v[152:155], v[192:195], 0
	v_mfma_f32_16x16x32_bf16 v[76:79], v[120:123], v[200:203], 0
	v_mfma_f32_16x16x32_bf16 v[72:75], v[152:155], v[200:203], 0
	v_mfma_f32_16x16x32_bf16 v[136:139], v[140:143], v[176:179], v[136:139]
	v_mfma_f32_16x16x32_bf16 v[132:135], v[156:159], v[176:179], v[132:135]
	v_mfma_f32_16x16x32_bf16 v[116:119], v[140:143], v[184:187], v[116:119]
	v_mfma_f32_16x16x32_bf16 v[112:115], v[156:159], v[184:187], v[112:115]
	v_mfma_f32_16x16x32_bf16 v[96:99], v[140:143], v[196:199], v[96:99]
	v_mfma_f32_16x16x32_bf16 v[92:95], v[156:159], v[196:199], v[92:95]
	v_mfma_f32_16x16x32_bf16 v[76:79], v[140:143], v[204:207], v[76:79]
	v_mfma_f32_16x16x32_bf16 v[72:75], v[156:159], v[204:207], v[72:75]
	s_barrier
	s_setprio 0
	s_mov_b32 m0, s23
	v_lshl_add_u64 v[188:189], s[24:25], 0, v[162:163]
	s_add_u32 s30, s24, 0x4000
	ds_read_b128 v[172:175], v191 offset:16384
	ds_read_b128 v[176:179], v191 offset:17408
	ds_read_b128 v[180:183], v191 offset:18432
	ds_read_b128 v[184:187], v191 offset:19456
	ds_read_b128 v[192:195], v191 offset:20480
	ds_read_b128 v[196:199], v191 offset:21504
	ds_read_b128 v[200:203], v191 offset:22528
	ds_read_b128 v[204:207], v191 offset:23552
	global_load_lds_dwordx4 v[188:189], off
	v_lshl_add_u64 v[188:189], s[24:25], 0, v[166:167]
	s_mov_b32 m0, s74
	s_addc_u32 s31, s25, 0
	global_load_lds_dwordx4 v[188:189], off
	v_lshl_add_u64 v[188:189], s[30:31], 0, v[162:163]
	s_mov_b32 m0, s76
	v_lshl_add_u64 v[208:209], s[38:39], 0, v[164:165]
	global_load_lds_dwordx4 v[188:189], off
	v_lshl_add_u64 v[188:189], s[30:31], 0, v[166:167]
	s_mov_b32 m0, s77
	s_nop 0
	global_load_lds_dwordx4 v[188:189], off
	v_lshl_add_u64 v[188:189], s[38:39], 0, v[160:161]
	s_mov_b32 m0, s78
	s_nop 0
	global_load_lds_dwordx4 v[188:189], off
	s_mov_b32 m0, s79
	s_nop 0
	global_load_lds_dwordx4 v[208:209], off
	s_waitcnt vmcnt(8)
	s_waitcnt lgkmcnt(0)
	s_setprio 1
	s_barrier
	v_mfma_f32_16x16x32_bf16 v[68:71], v[40:43], v[172:175], 0
	v_mfma_f32_16x16x32_bf16 v[64:67], v[80:83], v[172:175], 0
	v_mfma_f32_16x16x32_bf16 v[48:51], v[40:43], v[180:183], 0
	v_mfma_f32_16x16x32_bf16 v[44:47], v[80:83], v[180:183], 0
	v_mfma_f32_16x16x32_bf16 v[28:31], v[40:43], v[192:195], 0
	v_mfma_f32_16x16x32_bf16 v[24:27], v[80:83], v[192:195], 0
	v_mfma_f32_16x16x32_bf16 v[12:15], v[40:43], v[200:203], 0
	v_mfma_f32_16x16x32_bf16 v[8:11], v[80:83], v[200:203], 0
	v_mfma_f32_16x16x32_bf16 v[68:71], v[60:63], v[176:179], v[68:71]
	v_mfma_f32_16x16x32_bf16 v[64:67], v[100:103], v[176:179], v[64:67]
	v_mfma_f32_16x16x32_bf16 v[48:51], v[60:63], v[184:187], v[48:51]
	v_mfma_f32_16x16x32_bf16 v[44:47], v[100:103], v[184:187], v[44:47]
	v_mfma_f32_16x16x32_bf16 v[28:31], v[60:63], v[196:199], v[28:31]
	v_mfma_f32_16x16x32_bf16 v[24:27], v[100:103], v[196:199], v[24:27]
	v_mfma_f32_16x16x32_bf16 v[12:15], v[60:63], v[204:207], v[12:15]
	v_mfma_f32_16x16x32_bf16 v[8:11], v[100:103], v[204:207], v[8:11]
	v_mfma_f32_16x16x32_bf16 v[52:55], v[152:155], v[172:175], 0
	v_mfma_f32_16x16x32_bf16 v[36:39], v[120:123], v[180:183], 0
	v_mfma_f32_16x16x32_bf16 v[32:35], v[152:155], v[180:183], 0
	v_mfma_f32_16x16x32_bf16 v[20:23], v[120:123], v[192:195], 0
	v_mfma_f32_16x16x32_bf16 v[16:19], v[152:155], v[192:195], 0
	v_mfma_f32_16x16x32_bf16 v[4:7], v[120:123], v[200:203], 0
	v_mfma_f32_16x16x32_bf16 v[0:3], v[152:155], v[200:203], 0
	v_mfma_f32_16x16x32_bf16 v[40:43], v[120:123], v[172:175], 0
	v_mfma_f32_16x16x32_bf16 v[52:55], v[156:159], v[176:179], v[52:55]
	v_mfma_f32_16x16x32_bf16 v[36:39], v[140:143], v[184:187], v[36:39]
	v_mfma_f32_16x16x32_bf16 v[32:35], v[156:159], v[184:187], v[32:35]
	v_mfma_f32_16x16x32_bf16 v[20:23], v[140:143], v[196:199], v[20:23]
	v_mfma_f32_16x16x32_bf16 v[16:19], v[156:159], v[196:199], v[16:19]
	v_mfma_f32_16x16x32_bf16 v[4:7], v[140:143], v[204:207], v[4:7]
	v_mfma_f32_16x16x32_bf16 v[0:3], v[156:159], v[204:207], v[0:3]
	v_mfma_f32_16x16x32_bf16 v[40:43], v[140:143], v[176:179], v[40:43]
	s_barrier
	s_setprio 0
	v_add_u32_e32 v100, s86, v190
	v_add_u32_e32 v156, s95, v190
	ds_read_b128 v[56:59], v100
	ds_read_b128 v[60:63], v100 offset:1024
	ds_read_b128 v[80:83], v100 offset:2048
	ds_read_b128 v[100:103], v100 offset:3072
	ds_read_b128 v[120:123], v156
	ds_read_b128 v[140:143], v156 offset:1024
	ds_read_b128 v[152:155], v156 offset:2048
	ds_read_b128 v[156:159], v156 offset:3072
	s_add_u32 s30, s38, 0x80000
	s_addc_u32 s31, s39, 0
	s_mov_b32 m0, s82
	v_lshl_add_u64 v[210:211], s[30:31], 0, v[160:161]
	ds_read_b128 v[172:175], v191 offset:32768
	ds_read_b128 v[176:179], v191 offset:33792
	ds_read_b128 v[180:183], v191 offset:34816
	ds_read_b128 v[184:187], v191 offset:35840
	ds_read_b128 v[192:195], v191 offset:36864
	ds_read_b128 v[196:199], v191 offset:37888
	ds_read_b128 v[200:203], v191 offset:38912
	ds_read_b128 v[204:207], v191 offset:39936
	global_load_lds_dwordx4 v[210:211], off
	v_lshl_add_u64 v[210:211], s[30:31], 0, v[164:165]
	s_mov_b32 m0, s83
	s_nop 0
	global_load_lds_dwordx4 v[210:211], off
	s_waitcnt vmcnt(8)
	s_waitcnt lgkmcnt(0)
	s_setprio 1
	s_barrier
	v_mfma_f32_16x16x32_bf16 v[148:151], v[56:59], v[172:175], v[148:151]
	v_mfma_f32_16x16x32_bf16 v[144:147], v[80:83], v[172:175], v[144:147]
	v_mfma_f32_16x16x32_bf16 v[128:131], v[56:59], v[180:183], v[128:131]
	v_mfma_f32_16x16x32_bf16 v[124:127], v[80:83], v[180:183], v[124:127]
	v_mfma_f32_16x16x32_bf16 v[108:111], v[56:59], v[192:195], v[108:111]
	v_mfma_f32_16x16x32_bf16 v[104:107], v[80:83], v[192:195], v[104:107]
	v_mfma_f32_16x16x32_bf16 v[88:91], v[56:59], v[200:203], v[88:91]
	v_mfma_f32_16x16x32_bf16 v[84:87], v[80:83], v[200:203], v[84:87]
	v_mfma_f32_16x16x32_bf16 v[148:151], v[60:63], v[176:179], v[148:151]
	v_mfma_f32_16x16x32_bf16 v[144:147], v[100:103], v[176:179], v[144:147]
	v_mfma_f32_16x16x32_bf16 v[128:131], v[60:63], v[184:187], v[128:131]
	v_mfma_f32_16x16x32_bf16 v[124:127], v[100:103], v[184:187], v[124:127]
	v_mfma_f32_16x16x32_bf16 v[108:111], v[60:63], v[196:199], v[108:111]
	v_mfma_f32_16x16x32_bf16 v[104:107], v[100:103], v[196:199], v[104:107]
	v_mfma_f32_16x16x32_bf16 v[88:91], v[60:63], v[204:207], v[88:91]
	v_mfma_f32_16x16x32_bf16 v[84:87], v[100:103], v[204:207], v[84:87]
	v_mfma_f32_16x16x32_bf16 v[136:139], v[120:123], v[172:175], v[136:139]
	v_mfma_f32_16x16x32_bf16 v[132:135], v[152:155], v[172:175], v[132:135]
	v_mfma_f32_16x16x32_bf16 v[116:119], v[120:123], v[180:183], v[116:119]
	v_mfma_f32_16x16x32_bf16 v[112:115], v[152:155], v[180:183], v[112:115]
	v_mfma_f32_16x16x32_bf16 v[96:99], v[120:123], v[192:195], v[96:99]
	v_mfma_f32_16x16x32_bf16 v[92:95], v[152:155], v[192:195], v[92:95]
	v_mfma_f32_16x16x32_bf16 v[76:79], v[120:123], v[200:203], v[76:79]
	v_mfma_f32_16x16x32_bf16 v[72:75], v[152:155], v[200:203], v[72:75]
	v_mfma_f32_16x16x32_bf16 v[136:139], v[140:143], v[176:179], v[136:139]
	v_mfma_f32_16x16x32_bf16 v[132:135], v[156:159], v[176:179], v[132:135]
	v_mfma_f32_16x16x32_bf16 v[116:119], v[140:143], v[184:187], v[116:119]
	v_mfma_f32_16x16x32_bf16 v[112:115], v[156:159], v[184:187], v[112:115]
	v_mfma_f32_16x16x32_bf16 v[96:99], v[140:143], v[196:199], v[96:99]
	v_mfma_f32_16x16x32_bf16 v[92:95], v[156:159], v[196:199], v[92:95]
	v_mfma_f32_16x16x32_bf16 v[76:79], v[140:143], v[204:207], v[76:79]
	v_mfma_f32_16x16x32_bf16 v[72:75], v[156:159], v[204:207], v[72:75]
	s_barrier
	s_setprio 0
	s_add_u32 s30, s24, 0x8000
	s_addc_u32 s31, s25, 0
	s_mov_b32 m0, s87
	v_lshl_add_u64 v[210:211], s[30:31], 0, v[162:163]
	s_add_u32 s24, s24, 0xc000
	ds_read_b128 v[172:175], v191 offset:49152
	ds_read_b128 v[176:179], v191 offset:50176
	ds_read_b128 v[180:183], v191 offset:51200
	ds_read_b128 v[184:187], v191 offset:52224
	ds_read_b128 v[192:195], v191 offset:53248
	ds_read_b128 v[196:199], v191 offset:54272
	ds_read_b128 v[200:203], v191 offset:55296
	ds_read_b128 v[204:207], v191 offset:56320
	global_load_lds_dwordx4 v[210:211], off
	v_lshl_add_u64 v[210:211], s[30:31], 0, v[166:167]
	s_mov_b32 m0, s92
	s_addc_u32 s25, s25, 0
	global_load_lds_dwordx4 v[210:211], off
	v_lshl_add_u64 v[210:211], s[24:25], 0, v[162:163]
	s_mov_b32 m0, s96
	v_lshl_add_u64 v[188:189], v[188:189], 0, s[26:27]
	global_load_lds_dwordx4 v[210:211], off
	v_lshl_add_u64 v[210:211], s[24:25], 0, v[166:167]
	s_mov_b32 m0, s97
	s_nop 0
	global_load_lds_dwordx4 v[210:211], off
	s_mov_b32 m0, s93
	s_nop 0
	global_load_lds_dwordx4 v[188:189], off
	v_lshl_add_u64 v[188:189], v[208:209], 0, s[26:27]
	s_mov_b32 m0, s94
	s_nop 0
	global_load_lds_dwordx4 v[188:189], off
	s_waitcnt vmcnt(8)
	s_waitcnt lgkmcnt(0)
	s_setprio 1
	s_barrier
	v_mfma_f32_16x16x32_bf16 v[68:71], v[56:59], v[172:175], v[68:71]
	v_mfma_f32_16x16x32_bf16 v[64:67], v[80:83], v[172:175], v[64:67]
	v_mfma_f32_16x16x32_bf16 v[48:51], v[56:59], v[180:183], v[48:51]
	v_mfma_f32_16x16x32_bf16 v[44:47], v[80:83], v[180:183], v[44:47]
	v_mfma_f32_16x16x32_bf16 v[28:31], v[56:59], v[192:195], v[28:31]
	v_mfma_f32_16x16x32_bf16 v[24:27], v[80:83], v[192:195], v[24:27]
	v_mfma_f32_16x16x32_bf16 v[12:15], v[56:59], v[200:203], v[12:15]
	v_mfma_f32_16x16x32_bf16 v[8:11], v[80:83], v[200:203], v[8:11]
	v_mfma_f32_16x16x32_bf16 v[68:71], v[60:63], v[176:179], v[68:71]
	v_mfma_f32_16x16x32_bf16 v[64:67], v[100:103], v[176:179], v[64:67]
	v_mfma_f32_16x16x32_bf16 v[48:51], v[60:63], v[184:187], v[48:51]
	v_mfma_f32_16x16x32_bf16 v[44:47], v[100:103], v[184:187], v[44:47]
	v_mfma_f32_16x16x32_bf16 v[28:31], v[60:63], v[196:199], v[28:31]
	v_mfma_f32_16x16x32_bf16 v[24:27], v[100:103], v[196:199], v[24:27]
	v_mfma_f32_16x16x32_bf16 v[12:15], v[60:63], v[204:207], v[12:15]
	v_mfma_f32_16x16x32_bf16 v[8:11], v[100:103], v[204:207], v[8:11]
	v_mfma_f32_16x16x32_bf16 v[40:43], v[120:123], v[172:175], v[40:43]
	v_mfma_f32_16x16x32_bf16 v[56:59], v[140:143], v[176:179], v[40:43]
	v_mfma_f32_16x16x32_bf16 v[40:43], v[152:155], v[172:175], v[52:55]
	v_mfma_f32_16x16x32_bf16 v[36:39], v[120:123], v[180:183], v[36:39]
	v_mfma_f32_16x16x32_bf16 v[32:35], v[152:155], v[180:183], v[32:35]
	v_mfma_f32_16x16x32_bf16 v[20:23], v[120:123], v[192:195], v[20:23]
	v_mfma_f32_16x16x32_bf16 v[16:19], v[152:155], v[192:195], v[16:19]
	v_mfma_f32_16x16x32_bf16 v[4:7], v[120:123], v[200:203], v[4:7]
	v_mfma_f32_16x16x32_bf16 v[0:3], v[152:155], v[200:203], v[0:3]
	v_mfma_f32_16x16x32_bf16 v[52:55], v[156:159], v[176:179], v[40:43]
	v_mfma_f32_16x16x32_bf16 v[36:39], v[140:143], v[184:187], v[36:39]
	v_mfma_f32_16x16x32_bf16 v[32:35], v[156:159], v[184:187], v[32:35]
	v_mfma_f32_16x16x32_bf16 v[20:23], v[140:143], v[196:199], v[20:23]
	v_mfma_f32_16x16x32_bf16 v[16:19], v[156:159], v[196:199], v[16:19]
	v_mfma_f32_16x16x32_bf16 v[4:7], v[140:143], v[204:207], v[4:7]
	v_mfma_f32_16x16x32_bf16 v[0:3], v[156:159], v[204:207], v[0:3]
	s_barrier
	s_setprio 0
	s_add_i32 s28, s28, 2
	s_add_u32 s17, s17, 0x10000
	s_addc_u32 s19, s19, 0
	s_add_u32 s0, s0, 0x100
	s_addc_u32 s1, s1, 0
	s_cmp_gt_u32 s28, 29
.LBB0_311:
	v_add_u32_e32 v100, s3, v190
	v_add_u32_e32 v156, s75, v190
	ds_read_b128 v[40:43], v100
	ds_read_b128 v[60:63], v100 offset:1024
	ds_read_b128 v[80:83], v100 offset:2048
	ds_read_b128 v[100:103], v100 offset:3072
	ds_read_b128 v[120:123], v156
	ds_read_b128 v[140:143], v156 offset:1024
	ds_read_b128 v[152:155], v156 offset:2048
	ds_read_b128 v[156:159], v156 offset:3072
	s_add_u32 s24, s0, 0xfff80080
	s_addc_u32 s25, s1, -1
	s_cmp_eq_u32 s28, 28
	s_cselect_b32 s39, s4, s25
	s_cselect_b32 s38, s5, s24
	s_cselect_b32 s25, s8, s19
	s_cselect_b32 s24, s13, s17
	v_lshl_add_u64 v[188:189], s[0:1], 0, v[168:169]
	s_add_i32 m0, s78, 0xc000
	ds_read_b128 v[172:175], v191
	ds_read_b128 v[176:179], v191 offset:1024
	ds_read_b128 v[180:183], v191 offset:2048
	ds_read_b128 v[184:187], v191 offset:3072
	ds_read_b128 v[192:195], v191 offset:4096
	ds_read_b128 v[196:199], v191 offset:5120
	ds_read_b128 v[200:203], v191 offset:6144
	ds_read_b128 v[204:207], v191 offset:7168
	global_load_lds_dwordx4 v[188:189], off
	v_lshl_add_u64 v[188:189], s[0:1], 0, v[170:171]
	s_add_i32 m0, s78, 0xe000
	s_nop 0
	global_load_lds_dwordx4 v[188:189], off
	s_waitcnt vmcnt(8)
	s_waitcnt lgkmcnt(0)
	s_setprio 1
	s_barrier
	v_mfma_f32_16x16x32_bf16 v[148:151], v[40:43], v[172:175], v[148:151]
	v_mfma_f32_16x16x32_bf16 v[144:147], v[80:83], v[172:175], v[144:147]
	v_mfma_f32_16x16x32_bf16 v[128:131], v[40:43], v[180:183], v[128:131]
	v_mfma_f32_16x16x32_bf16 v[124:127], v[80:83], v[180:183], v[124:127]
	v_mfma_f32_16x16x32_bf16 v[108:111], v[40:43], v[192:195], v[108:111]
	v_mfma_f32_16x16x32_bf16 v[104:107], v[80:83], v[192:195], v[104:107]
	v_mfma_f32_16x16x32_bf16 v[88:91], v[40:43], v[200:203], v[88:91]
	v_mfma_f32_16x16x32_bf16 v[84:87], v[80:83], v[200:203], v[84:87]
	v_mfma_f32_16x16x32_bf16 v[148:151], v[60:63], v[176:179], v[148:151]
	v_mfma_f32_16x16x32_bf16 v[144:147], v[100:103], v[176:179], v[144:147]
	v_mfma_f32_16x16x32_bf16 v[128:131], v[60:63], v[184:187], v[128:131]
	v_mfma_f32_16x16x32_bf16 v[124:127], v[100:103], v[184:187], v[124:127]
	v_mfma_f32_16x16x32_bf16 v[108:111], v[60:63], v[196:199], v[108:111]
	v_mfma_f32_16x16x32_bf16 v[104:107], v[100:103], v[196:199], v[104:107]
	v_mfma_f32_16x16x32_bf16 v[88:91], v[60:63], v[204:207], v[88:91]
	v_mfma_f32_16x16x32_bf16 v[84:87], v[100:103], v[204:207], v[84:87]
	v_mfma_f32_16x16x32_bf16 v[136:139], v[120:123], v[172:175], v[136:139]
	v_mfma_f32_16x16x32_bf16 v[132:135], v[152:155], v[172:175], v[132:135]
	v_mfma_f32_16x16x32_bf16 v[116:119], v[120:123], v[180:183], v[116:119]
	v_mfma_f32_16x16x32_bf16 v[112:115], v[152:155], v[180:183], v[112:115]
	v_mfma_f32_16x16x32_bf16 v[96:99], v[120:123], v[192:195], v[96:99]
	v_mfma_f32_16x16x32_bf16 v[92:95], v[152:155], v[192:195], v[92:95]
	v_mfma_f32_16x16x32_bf16 v[76:79], v[120:123], v[200:203], v[76:79]
	v_mfma_f32_16x16x32_bf16 v[72:75], v[152:155], v[200:203], v[72:75]
	v_mfma_f32_16x16x32_bf16 v[136:139], v[140:143], v[176:179], v[136:139]
	v_mfma_f32_16x16x32_bf16 v[132:135], v[156:159], v[176:179], v[132:135]
	v_mfma_f32_16x16x32_bf16 v[116:119], v[140:143], v[184:187], v[116:119]
	v_mfma_f32_16x16x32_bf16 v[112:115], v[156:159], v[184:187], v[112:115]
	v_mfma_f32_16x16x32_bf16 v[96:99], v[140:143], v[196:199], v[96:99]
	v_mfma_f32_16x16x32_bf16 v[92:95], v[156:159], v[196:199], v[92:95]
	v_mfma_f32_16x16x32_bf16 v[76:79], v[140:143], v[204:207], v[76:79]
	v_mfma_f32_16x16x32_bf16 v[72:75], v[156:159], v[204:207], v[72:75]
	s_barrier
	s_setprio 0
	s_mov_b32 m0, s23
	v_lshl_add_u64 v[188:189], s[24:25], 0, v[162:163]
	s_add_u32 s30, s24, 0x4000
	ds_read_b128 v[172:175], v191 offset:16384
	ds_read_b128 v[176:179], v191 offset:17408
	ds_read_b128 v[180:183], v191 offset:18432
	ds_read_b128 v[184:187], v191 offset:19456
	ds_read_b128 v[192:195], v191 offset:20480
	ds_read_b128 v[196:199], v191 offset:21504
	ds_read_b128 v[200:203], v191 offset:22528
	ds_read_b128 v[204:207], v191 offset:23552
	global_load_lds_dwordx4 v[188:189], off
	v_lshl_add_u64 v[188:189], s[24:25], 0, v[166:167]
	s_mov_b32 m0, s74
	s_addc_u32 s31, s25, 0
	global_load_lds_dwordx4 v[188:189], off
	v_lshl_add_u64 v[188:189], s[30:31], 0, v[162:163]
	s_mov_b32 m0, s76
	v_lshl_add_u64 v[208:209], s[38:39], 0, v[164:165]
	global_load_lds_dwordx4 v[188:189], off
	v_lshl_add_u64 v[188:189], s[30:31], 0, v[166:167]
	s_mov_b32 m0, s77
	s_nop 0
	global_load_lds_dwordx4 v[188:189], off
	v_lshl_add_u64 v[188:189], s[38:39], 0, v[160:161]
	s_mov_b32 m0, s78
	s_nop 0
	global_load_lds_dwordx4 v[188:189], off
	s_mov_b32 m0, s79
	s_nop 0
	global_load_lds_dwordx4 v[208:209], off
	s_waitcnt vmcnt(8)
	s_waitcnt lgkmcnt(0)
	s_setprio 1
	s_barrier
	v_mfma_f32_16x16x32_bf16 v[68:71], v[40:43], v[172:175], v[68:71]
	v_mfma_f32_16x16x32_bf16 v[64:67], v[80:83], v[172:175], v[64:67]
	v_mfma_f32_16x16x32_bf16 v[48:51], v[40:43], v[180:183], v[48:51]
	v_mfma_f32_16x16x32_bf16 v[44:47], v[80:83], v[180:183], v[44:47]
	v_mfma_f32_16x16x32_bf16 v[28:31], v[40:43], v[192:195], v[28:31]
	v_mfma_f32_16x16x32_bf16 v[24:27], v[80:83], v[192:195], v[24:27]
	v_mfma_f32_16x16x32_bf16 v[12:15], v[40:43], v[200:203], v[12:15]
	v_mfma_f32_16x16x32_bf16 v[8:11], v[80:83], v[200:203], v[8:11]
	v_mfma_f32_16x16x32_bf16 v[68:71], v[60:63], v[176:179], v[68:71]
	v_mfma_f32_16x16x32_bf16 v[64:67], v[100:103], v[176:179], v[64:67]
	v_mfma_f32_16x16x32_bf16 v[48:51], v[60:63], v[184:187], v[48:51]
	v_mfma_f32_16x16x32_bf16 v[44:47], v[100:103], v[184:187], v[44:47]
	v_mfma_f32_16x16x32_bf16 v[28:31], v[60:63], v[196:199], v[28:31]
	v_mfma_f32_16x16x32_bf16 v[24:27], v[100:103], v[196:199], v[24:27]
	v_mfma_f32_16x16x32_bf16 v[12:15], v[60:63], v[204:207], v[12:15]
	v_mfma_f32_16x16x32_bf16 v[8:11], v[100:103], v[204:207], v[8:11]
	v_mfma_f32_16x16x32_bf16 v[52:55], v[152:155], v[172:175], v[52:55]
	v_mfma_f32_16x16x32_bf16 v[36:39], v[120:123], v[180:183], v[36:39]
	v_mfma_f32_16x16x32_bf16 v[32:35], v[152:155], v[180:183], v[32:35]
	v_mfma_f32_16x16x32_bf16 v[20:23], v[120:123], v[192:195], v[20:23]
	v_mfma_f32_16x16x32_bf16 v[16:19], v[152:155], v[192:195], v[16:19]
	v_mfma_f32_16x16x32_bf16 v[4:7], v[120:123], v[200:203], v[4:7]
	v_mfma_f32_16x16x32_bf16 v[0:3], v[152:155], v[200:203], v[0:3]
	v_mfma_f32_16x16x32_bf16 v[40:43], v[120:123], v[172:175], v[56:59]
	v_mfma_f32_16x16x32_bf16 v[52:55], v[156:159], v[176:179], v[52:55]
	v_mfma_f32_16x16x32_bf16 v[36:39], v[140:143], v[184:187], v[36:39]
	v_mfma_f32_16x16x32_bf16 v[32:35], v[156:159], v[184:187], v[32:35]
	v_mfma_f32_16x16x32_bf16 v[20:23], v[140:143], v[196:199], v[20:23]
	v_mfma_f32_16x16x32_bf16 v[16:19], v[156:159], v[196:199], v[16:19]
	v_mfma_f32_16x16x32_bf16 v[4:7], v[140:143], v[204:207], v[4:7]
	v_mfma_f32_16x16x32_bf16 v[0:3], v[156:159], v[204:207], v[0:3]
	v_mfma_f32_16x16x32_bf16 v[40:43], v[140:143], v[176:179], v[40:43]
	s_barrier
	s_setprio 0
	v_add_u32_e32 v100, s86, v190
	v_add_u32_e32 v156, s95, v190
	ds_read_b128 v[56:59], v100
	ds_read_b128 v[60:63], v100 offset:1024
	ds_read_b128 v[80:83], v100 offset:2048
	ds_read_b128 v[100:103], v100 offset:3072
	ds_read_b128 v[120:123], v156
	ds_read_b128 v[140:143], v156 offset:1024
	ds_read_b128 v[152:155], v156 offset:2048
	ds_read_b128 v[156:159], v156 offset:3072
	s_add_u32 s30, s38, 0x80000
	s_addc_u32 s31, s39, 0
	s_mov_b32 m0, s82
	v_lshl_add_u64 v[210:211], s[30:31], 0, v[160:161]
	ds_read_b128 v[172:175], v191 offset:32768
	ds_read_b128 v[176:179], v191 offset:33792
	ds_read_b128 v[180:183], v191 offset:34816
	ds_read_b128 v[184:187], v191 offset:35840
	ds_read_b128 v[192:195], v191 offset:36864
	ds_read_b128 v[196:199], v191 offset:37888
	ds_read_b128 v[200:203], v191 offset:38912
	ds_read_b128 v[204:207], v191 offset:39936
	global_load_lds_dwordx4 v[210:211], off
	v_lshl_add_u64 v[210:211], s[30:31], 0, v[164:165]
	s_mov_b32 m0, s83
	s_nop 0
	global_load_lds_dwordx4 v[210:211], off
	s_waitcnt vmcnt(8)
	s_waitcnt lgkmcnt(0)
	s_setprio 1
	s_barrier
	v_mfma_f32_16x16x32_bf16 v[148:151], v[56:59], v[172:175], v[148:151]
	v_mfma_f32_16x16x32_bf16 v[144:147], v[80:83], v[172:175], v[144:147]
	v_mfma_f32_16x16x32_bf16 v[128:131], v[56:59], v[180:183], v[128:131]
	v_mfma_f32_16x16x32_bf16 v[124:127], v[80:83], v[180:183], v[124:127]
	v_mfma_f32_16x16x32_bf16 v[108:111], v[56:59], v[192:195], v[108:111]
	v_mfma_f32_16x16x32_bf16 v[104:107], v[80:83], v[192:195], v[104:107]
	v_mfma_f32_16x16x32_bf16 v[88:91], v[56:59], v[200:203], v[88:91]
	v_mfma_f32_16x16x32_bf16 v[84:87], v[80:83], v[200:203], v[84:87]
	v_mfma_f32_16x16x32_bf16 v[148:151], v[60:63], v[176:179], v[148:151]
	v_mfma_f32_16x16x32_bf16 v[144:147], v[100:103], v[176:179], v[144:147]
	v_mfma_f32_16x16x32_bf16 v[128:131], v[60:63], v[184:187], v[128:131]
	v_mfma_f32_16x16x32_bf16 v[124:127], v[100:103], v[184:187], v[124:127]
	v_mfma_f32_16x16x32_bf16 v[108:111], v[60:63], v[196:199], v[108:111]
	v_mfma_f32_16x16x32_bf16 v[104:107], v[100:103], v[196:199], v[104:107]
	v_mfma_f32_16x16x32_bf16 v[88:91], v[60:63], v[204:207], v[88:91]
	v_mfma_f32_16x16x32_bf16 v[84:87], v[100:103], v[204:207], v[84:87]
	v_mfma_f32_16x16x32_bf16 v[136:139], v[120:123], v[172:175], v[136:139]
	v_mfma_f32_16x16x32_bf16 v[132:135], v[152:155], v[172:175], v[132:135]
	v_mfma_f32_16x16x32_bf16 v[116:119], v[120:123], v[180:183], v[116:119]
	v_mfma_f32_16x16x32_bf16 v[112:115], v[152:155], v[180:183], v[112:115]
	v_mfma_f32_16x16x32_bf16 v[96:99], v[120:123], v[192:195], v[96:99]
	v_mfma_f32_16x16x32_bf16 v[92:95], v[152:155], v[192:195], v[92:95]
	v_mfma_f32_16x16x32_bf16 v[76:79], v[120:123], v[200:203], v[76:79]
	v_mfma_f32_16x16x32_bf16 v[72:75], v[152:155], v[200:203], v[72:75]
	v_mfma_f32_16x16x32_bf16 v[136:139], v[140:143], v[176:179], v[136:139]
	v_mfma_f32_16x16x32_bf16 v[132:135], v[156:159], v[176:179], v[132:135]
	v_mfma_f32_16x16x32_bf16 v[116:119], v[140:143], v[184:187], v[116:119]
	v_mfma_f32_16x16x32_bf16 v[112:115], v[156:159], v[184:187], v[112:115]
	v_mfma_f32_16x16x32_bf16 v[96:99], v[140:143], v[196:199], v[96:99]
	v_mfma_f32_16x16x32_bf16 v[92:95], v[156:159], v[196:199], v[92:95]
	v_mfma_f32_16x16x32_bf16 v[76:79], v[140:143], v[204:207], v[76:79]
	v_mfma_f32_16x16x32_bf16 v[72:75], v[156:159], v[204:207], v[72:75]
	s_barrier
	s_setprio 0
	s_add_u32 s30, s24, 0x8000
	s_addc_u32 s31, s25, 0
	s_mov_b32 m0, s87
	v_lshl_add_u64 v[210:211], s[30:31], 0, v[162:163]
	s_add_u32 s24, s24, 0xc000
	ds_read_b128 v[172:175], v191 offset:49152
	ds_read_b128 v[176:179], v191 offset:50176
	ds_read_b128 v[180:183], v191 offset:51200
	ds_read_b128 v[184:187], v191 offset:52224
	ds_read_b128 v[192:195], v191 offset:53248
	ds_read_b128 v[196:199], v191 offset:54272
	ds_read_b128 v[200:203], v191 offset:55296
	ds_read_b128 v[204:207], v191 offset:56320
	global_load_lds_dwordx4 v[210:211], off
	v_lshl_add_u64 v[210:211], s[30:31], 0, v[166:167]
	s_mov_b32 m0, s92
	s_addc_u32 s25, s25, 0
	global_load_lds_dwordx4 v[210:211], off
	v_lshl_add_u64 v[210:211], s[24:25], 0, v[162:163]
	s_mov_b32 m0, s96
	v_lshl_add_u64 v[188:189], v[188:189], 0, s[26:27]
	global_load_lds_dwordx4 v[210:211], off
	v_lshl_add_u64 v[210:211], s[24:25], 0, v[166:167]
	s_mov_b32 m0, s97
	s_nop 0
	global_load_lds_dwordx4 v[210:211], off
	s_mov_b32 m0, s93
	s_nop 0
	global_load_lds_dwordx4 v[188:189], off
	v_lshl_add_u64 v[188:189], v[208:209], 0, s[26:27]
	s_mov_b32 m0, s94
	s_nop 0
	global_load_lds_dwordx4 v[188:189], off
	s_waitcnt vmcnt(8)
	s_waitcnt lgkmcnt(0)
	s_setprio 1
	s_barrier
	v_mfma_f32_16x16x32_bf16 v[68:71], v[56:59], v[172:175], v[68:71]
	v_mfma_f32_16x16x32_bf16 v[64:67], v[80:83], v[172:175], v[64:67]
	v_mfma_f32_16x16x32_bf16 v[48:51], v[56:59], v[180:183], v[48:51]
	v_mfma_f32_16x16x32_bf16 v[44:47], v[80:83], v[180:183], v[44:47]
	v_mfma_f32_16x16x32_bf16 v[28:31], v[56:59], v[192:195], v[28:31]
	v_mfma_f32_16x16x32_bf16 v[24:27], v[80:83], v[192:195], v[24:27]
	v_mfma_f32_16x16x32_bf16 v[12:15], v[56:59], v[200:203], v[12:15]
	v_mfma_f32_16x16x32_bf16 v[8:11], v[80:83], v[200:203], v[8:11]
	v_mfma_f32_16x16x32_bf16 v[68:71], v[60:63], v[176:179], v[68:71]
	v_mfma_f32_16x16x32_bf16 v[64:67], v[100:103], v[176:179], v[64:67]
	v_mfma_f32_16x16x32_bf16 v[48:51], v[60:63], v[184:187], v[48:51]
	v_mfma_f32_16x16x32_bf16 v[44:47], v[100:103], v[184:187], v[44:47]
	v_mfma_f32_16x16x32_bf16 v[28:31], v[60:63], v[196:199], v[28:31]
	v_mfma_f32_16x16x32_bf16 v[24:27], v[100:103], v[196:199], v[24:27]
	v_mfma_f32_16x16x32_bf16 v[12:15], v[60:63], v[204:207], v[12:15]
	v_mfma_f32_16x16x32_bf16 v[8:11], v[100:103], v[204:207], v[8:11]
	v_mfma_f32_16x16x32_bf16 v[40:43], v[120:123], v[172:175], v[40:43]
	v_mfma_f32_16x16x32_bf16 v[56:59], v[140:143], v[176:179], v[40:43]
	v_mfma_f32_16x16x32_bf16 v[40:43], v[152:155], v[172:175], v[52:55]
	v_mfma_f32_16x16x32_bf16 v[36:39], v[120:123], v[180:183], v[36:39]
	v_mfma_f32_16x16x32_bf16 v[32:35], v[152:155], v[180:183], v[32:35]
	v_mfma_f32_16x16x32_bf16 v[20:23], v[120:123], v[192:195], v[20:23]
	v_mfma_f32_16x16x32_bf16 v[16:19], v[152:155], v[192:195], v[16:19]
	v_mfma_f32_16x16x32_bf16 v[4:7], v[120:123], v[200:203], v[4:7]
	v_mfma_f32_16x16x32_bf16 v[0:3], v[152:155], v[200:203], v[0:3]
	v_mfma_f32_16x16x32_bf16 v[52:55], v[156:159], v[176:179], v[40:43]
	v_mfma_f32_16x16x32_bf16 v[36:39], v[140:143], v[184:187], v[36:39]
	v_mfma_f32_16x16x32_bf16 v[32:35], v[156:159], v[184:187], v[32:35]
	v_mfma_f32_16x16x32_bf16 v[20:23], v[140:143], v[196:199], v[20:23]
	v_mfma_f32_16x16x32_bf16 v[16:19], v[156:159], v[196:199], v[16:19]
	v_mfma_f32_16x16x32_bf16 v[4:7], v[140:143], v[204:207], v[4:7]
	v_mfma_f32_16x16x32_bf16 v[0:3], v[156:159], v[204:207], v[0:3]
	s_barrier
	s_setprio 0
	s_add_i32 s28, s28, 2
	s_add_u32 s17, s17, 0x10000
	s_addc_u32 s19, s19, 0
	s_add_u32 s0, s0, 0x100
	s_addc_u32 s1, s1, 0
	s_cmp_gt_u32 s28, 29
	s_cbranch_scc0 .LBB0_311
	s_and_b64 vcc, exec, s[34:35]
	s_cbranch_vccz .LBB0_314
	s_barrier

.LBB0_1054:
	s_ashr_i32 s41, s40, 31
	s_lshl_b64 s[4:5], s[40:41], 20
	s_add_u32 s44, s16, s4
	s_addc_u32 s45, s17, s5
	s_and_b64 s[4:5], s[36:37], exec
	s_cselect_b32 s4, s45, s51
	s_cselect_b32 s5, s44, s50
	s_ashr_i32 s39, s38, 31
	s_lshl_b64 s[46:47], s[38:39], 20
	s_add_u32 s46, s18, s46
	s_addc_u32 s47, s19, s47
	s_and_b64 s[52:53], s[36:37], exec
	s_cselect_b32 s39, s47, s1
	s_cselect_b32 s41, s46, s0
	s_add_u32 s49, s0, 0x10000
	s_addc_u32 s55, s1, 0
	s_add_u32 s0, s50, 0x80080
	s_addc_u32 s1, s51, 0
	s_mov_b32 s80, -2
	v_add_u32_e32 v140, s28, v215
	v_add_u32_e32 v156, s54, v215
	ds_read_b128 v[128:131], v140
	ds_read_b128 v[132:135], v140 offset:1024
	ds_read_b128 v[136:139], v140 offset:2048
	ds_read_b128 v[140:143], v140 offset:3072
	ds_read_b128 v[144:147], v156
	ds_read_b128 v[148:151], v156 offset:1024
	ds_read_b128 v[152:155], v156 offset:2048
	ds_read_b128 v[156:159], v156 offset:3072
	s_add_u32 s50, s0, 0xfff80080
	s_addc_u32 s51, s1, -1
	s_cmp_eq_u32 s80, 28
	s_cselect_b32 s53, s4, s51
	s_cselect_b32 s52, s5, s50
	s_cselect_b32 s51, s39, s55
	s_cselect_b32 s50, s41, s49
	v_lshl_add_u64 v[204:205], s[0:1], 0, v[180:181]
	s_add_i32 m0, s58, 0xc000
	ds_read_b128 v[160:163], v251
	ds_read_b128 v[164:167], v251 offset:1024
	ds_read_b128 v[168:171], v251 offset:2048
	ds_read_b128 v[184:187], v251 offset:3072
	ds_read_b128 v[188:191], v251 offset:4096
	ds_read_b128 v[192:195], v251 offset:5120
	ds_read_b128 v[196:199], v251 offset:6144
	ds_read_b128 v[200:203], v251 offset:7168
	global_load_lds_dwordx4 v[204:205], off
	v_lshl_add_u64 v[204:205], s[0:1], 0, v[182:183]
	s_add_i32 m0, s58, 0xe000
	s_nop 0
	global_load_lds_dwordx4 v[204:205], off
	s_waitcnt vmcnt(8)
	s_waitcnt lgkmcnt(0)
	s_setprio 1
	s_barrier
	v_mfma_f32_16x16x32_bf16 v[124:127], v[128:131], v[160:163], 0
	v_mfma_f32_16x16x32_bf16 v[120:123], v[136:139], v[160:163], 0
	v_mfma_f32_16x16x32_bf16 v[116:119], v[128:131], v[168:171], 0
	v_mfma_f32_16x16x32_bf16 v[112:115], v[136:139], v[168:171], 0
	v_mfma_f32_16x16x32_bf16 v[108:111], v[128:131], v[188:191], 0
	v_mfma_f32_16x16x32_bf16 v[104:107], v[136:139], v[188:191], 0
	v_mfma_f32_16x16x32_bf16 v[100:103], v[128:131], v[196:199], 0
	v_mfma_f32_16x16x32_bf16 v[96:99], v[136:139], v[196:199], 0
	v_mfma_f32_16x16x32_bf16 v[124:127], v[132:135], v[164:167], v[124:127]
	v_mfma_f32_16x16x32_bf16 v[120:123], v[140:143], v[164:167], v[120:123]
	v_mfma_f32_16x16x32_bf16 v[116:119], v[132:135], v[184:187], v[116:119]
	v_mfma_f32_16x16x32_bf16 v[112:115], v[140:143], v[184:187], v[112:115]
	v_mfma_f32_16x16x32_bf16 v[108:111], v[132:135], v[192:195], v[108:111]
	v_mfma_f32_16x16x32_bf16 v[104:107], v[140:143], v[192:195], v[104:107]
	v_mfma_f32_16x16x32_bf16 v[100:103], v[132:135], v[200:203], v[100:103]
	v_mfma_f32_16x16x32_bf16 v[96:99], v[140:143], v[200:203], v[96:99]
	v_mfma_f32_16x16x32_bf16 v[60:63], v[144:147], v[160:163], 0
	v_mfma_f32_16x16x32_bf16 v[56:59], v[152:155], v[160:163], 0
	v_mfma_f32_16x16x32_bf16 v[52:55], v[144:147], v[168:171], 0
	v_mfma_f32_16x16x32_bf16 v[48:51], v[152:155], v[168:171], 0
	v_mfma_f32_16x16x32_bf16 v[44:47], v[144:147], v[188:191], 0
	v_mfma_f32_16x16x32_bf16 v[40:43], v[152:155], v[188:191], 0
	v_mfma_f32_16x16x32_bf16 v[36:39], v[144:147], v[196:199], 0
	v_mfma_f32_16x16x32_bf16 v[32:35], v[152:155], v[196:199], 0
	v_mfma_f32_16x16x32_bf16 v[60:63], v[148:151], v[164:167], v[60:63]
	v_mfma_f32_16x16x32_bf16 v[56:59], v[156:159], v[164:167], v[56:59]
	v_mfma_f32_16x16x32_bf16 v[52:55], v[148:151], v[184:187], v[52:55]
	v_mfma_f32_16x16x32_bf16 v[48:51], v[156:159], v[184:187], v[48:51]
	v_mfma_f32_16x16x32_bf16 v[44:47], v[148:151], v[192:195], v[44:47]
	v_mfma_f32_16x16x32_bf16 v[40:43], v[156:159], v[192:195], v[40:43]
	v_mfma_f32_16x16x32_bf16 v[36:39], v[148:151], v[200:203], v[36:39]
	v_mfma_f32_16x16x32_bf16 v[32:35], v[156:159], v[200:203], v[32:35]
	s_barrier
	s_setprio 0
	s_mov_b32 m0, s30
	v_lshl_add_u64 v[204:205], s[50:51], 0, v[174:175]
	s_add_u32 s82, s50, 0x4000
	ds_read_b128 v[160:163], v251 offset:16384
	ds_read_b128 v[164:167], v251 offset:17408
	ds_read_b128 v[168:171], v251 offset:18432
	ds_read_b128 v[184:187], v251 offset:19456
	ds_read_b128 v[188:191], v251 offset:20480
	ds_read_b128 v[192:195], v251 offset:21504
	ds_read_b128 v[196:199], v251 offset:22528
	ds_read_b128 v[200:203], v251 offset:23552
	global_load_lds_dwordx4 v[204:205], off
	v_lshl_add_u64 v[204:205], s[50:51], 0, v[178:179]
	s_mov_b32 m0, s43
	s_addc_u32 s83, s51, 0
	global_load_lds_dwordx4 v[204:205], off
	v_lshl_add_u64 v[204:205], s[82:83], 0, v[174:175]
	s_mov_b32 m0, s56
	v_lshl_add_u64 v[206:207], s[52:53], 0, v[176:177]
	global_load_lds_dwordx4 v[204:205], off
	v_lshl_add_u64 v[204:205], s[82:83], 0, v[178:179]
	s_mov_b32 m0, s57
	s_nop 0
	global_load_lds_dwordx4 v[204:205], off
	v_lshl_add_u64 v[204:205], s[52:53], 0, v[172:173]
	s_mov_b32 m0, s58
	s_nop 0
	global_load_lds_dwordx4 v[204:205], off
	s_mov_b32 m0, s59
	s_nop 0
	global_load_lds_dwordx4 v[206:207], off
	s_waitcnt vmcnt(8)
	s_waitcnt lgkmcnt(0)
	s_setprio 1
	s_barrier
	v_mfma_f32_16x16x32_bf16 v[92:95], v[128:131], v[160:163], 0
	v_mfma_f32_16x16x32_bf16 v[88:91], v[136:139], v[160:163], 0
	v_mfma_f32_16x16x32_bf16 v[84:87], v[128:131], v[168:171], 0
	v_mfma_f32_16x16x32_bf16 v[80:83], v[136:139], v[168:171], 0
	v_mfma_f32_16x16x32_bf16 v[76:79], v[128:131], v[188:191], 0
	v_mfma_f32_16x16x32_bf16 v[72:75], v[136:139], v[188:191], 0
	v_mfma_f32_16x16x32_bf16 v[68:71], v[128:131], v[196:199], 0
	v_mfma_f32_16x16x32_bf16 v[64:67], v[136:139], v[196:199], 0
	v_mfma_f32_16x16x32_bf16 v[92:95], v[132:135], v[164:167], v[92:95]
	v_mfma_f32_16x16x32_bf16 v[88:91], v[140:143], v[164:167], v[88:91]
	v_mfma_f32_16x16x32_bf16 v[84:87], v[132:135], v[184:187], v[84:87]
	v_mfma_f32_16x16x32_bf16 v[80:83], v[140:143], v[184:187], v[80:83]
	v_mfma_f32_16x16x32_bf16 v[76:79], v[132:135], v[192:195], v[76:79]
	v_mfma_f32_16x16x32_bf16 v[72:75], v[140:143], v[192:195], v[72:75]
	v_mfma_f32_16x16x32_bf16 v[68:71], v[132:135], v[200:203], v[68:71]
	v_mfma_f32_16x16x32_bf16 v[64:67], v[140:143], v[200:203], v[64:67]
	v_mfma_f32_16x16x32_bf16 v[28:31], v[144:147], v[160:163], 0
	v_mfma_f32_16x16x32_bf16 v[24:27], v[152:155], v[160:163], 0
	v_mfma_f32_16x16x32_bf16 v[20:23], v[144:147], v[168:171], 0
	v_mfma_f32_16x16x32_bf16 v[16:19], v[152:155], v[168:171], 0
	v_mfma_f32_16x16x32_bf16 v[12:15], v[144:147], v[188:191], 0
	v_mfma_f32_16x16x32_bf16 v[8:11], v[152:155], v[188:191], 0
	v_mfma_f32_16x16x32_bf16 v[4:7], v[144:147], v[196:199], 0
	v_mfma_f32_16x16x32_bf16 v[0:3], v[152:155], v[196:199], 0
	v_mfma_f32_16x16x32_bf16 v[28:31], v[148:151], v[164:167], v[28:31]
	v_mfma_f32_16x16x32_bf16 v[24:27], v[156:159], v[164:167], v[24:27]
	v_mfma_f32_16x16x32_bf16 v[20:23], v[148:151], v[184:187], v[20:23]
	v_mfma_f32_16x16x32_bf16 v[16:19], v[156:159], v[184:187], v[16:19]
	v_mfma_f32_16x16x32_bf16 v[12:15], v[148:151], v[192:195], v[12:15]
	v_mfma_f32_16x16x32_bf16 v[8:11], v[156:159], v[192:195], v[8:11]
	v_mfma_f32_16x16x32_bf16 v[4:7], v[148:151], v[200:203], v[4:7]
	v_mfma_f32_16x16x32_bf16 v[0:3], v[156:159], v[200:203], v[0:3]
	s_barrier
	s_setprio 0
	v_add_u32_e32 v140, s68, v215
	v_add_u32_e32 v156, s73, v215
	ds_read_b128 v[128:131], v140
	ds_read_b128 v[132:135], v140 offset:1024
	ds_read_b128 v[136:139], v140 offset:2048
	ds_read_b128 v[140:143], v140 offset:3072
	ds_read_b128 v[144:147], v156
	ds_read_b128 v[148:151], v156 offset:1024
	ds_read_b128 v[152:155], v156 offset:2048
	ds_read_b128 v[156:159], v156 offset:3072
	s_add_u32 s52, s52, 0x80000
	s_addc_u32 s53, s53, 0
	s_mov_b32 m0, s60
	v_lshl_add_u64 v[208:209], s[52:53], 0, v[172:173]
	ds_read_b128 v[160:163], v251 offset:32768
	ds_read_b128 v[164:167], v251 offset:33792
	ds_read_b128 v[168:171], v251 offset:34816
	ds_read_b128 v[184:187], v251 offset:35840
	ds_read_b128 v[188:191], v251 offset:36864
	ds_read_b128 v[192:195], v251 offset:37888
	ds_read_b128 v[196:199], v251 offset:38912
	ds_read_b128 v[200:203], v251 offset:39936
	global_load_lds_dwordx4 v[208:209], off
	v_lshl_add_u64 v[208:209], s[52:53], 0, v[176:177]
	s_mov_b32 m0, s61
	s_nop 0
	global_load_lds_dwordx4 v[208:209], off
	s_waitcnt vmcnt(8)
	s_waitcnt lgkmcnt(0)
	s_setprio 1
	s_barrier
	v_mfma_f32_16x16x32_bf16 v[124:127], v[128:131], v[160:163], v[124:127]
	v_mfma_f32_16x16x32_bf16 v[120:123], v[136:139], v[160:163], v[120:123]
	v_mfma_f32_16x16x32_bf16 v[116:119], v[128:131], v[168:171], v[116:119]
	v_mfma_f32_16x16x32_bf16 v[112:115], v[136:139], v[168:171], v[112:115]
	v_mfma_f32_16x16x32_bf16 v[108:111], v[128:131], v[188:191], v[108:111]
	v_mfma_f32_16x16x32_bf16 v[104:107], v[136:139], v[188:191], v[104:107]
	v_mfma_f32_16x16x32_bf16 v[100:103], v[128:131], v[196:199], v[100:103]
	v_mfma_f32_16x16x32_bf16 v[96:99], v[136:139], v[196:199], v[96:99]
	v_mfma_f32_16x16x32_bf16 v[124:127], v[132:135], v[164:167], v[124:127]
	v_mfma_f32_16x16x32_bf16 v[120:123], v[140:143], v[164:167], v[120:123]
	v_mfma_f32_16x16x32_bf16 v[116:119], v[132:135], v[184:187], v[116:119]
	v_mfma_f32_16x16x32_bf16 v[112:115], v[140:143], v[184:187], v[112:115]
	v_mfma_f32_16x16x32_bf16 v[108:111], v[132:135], v[192:195], v[108:111]
	v_mfma_f32_16x16x32_bf16 v[104:107], v[140:143], v[192:195], v[104:107]
	v_mfma_f32_16x16x32_bf16 v[100:103], v[132:135], v[200:203], v[100:103]
	v_mfma_f32_16x16x32_bf16 v[96:99], v[140:143], v[200:203], v[96:99]
	v_mfma_f32_16x16x32_bf16 v[60:63], v[144:147], v[160:163], v[60:63]
	v_mfma_f32_16x16x32_bf16 v[56:59], v[152:155], v[160:163], v[56:59]
	v_mfma_f32_16x16x32_bf16 v[52:55], v[144:147], v[168:171], v[52:55]
	v_mfma_f32_16x16x32_bf16 v[48:51], v[152:155], v[168:171], v[48:51]
	v_mfma_f32_16x16x32_bf16 v[44:47], v[144:147], v[188:191], v[44:47]
	v_mfma_f32_16x16x32_bf16 v[40:43], v[152:155], v[188:191], v[40:43]
	v_mfma_f32_16x16x32_bf16 v[36:39], v[144:147], v[196:199], v[36:39]
	v_mfma_f32_16x16x32_bf16 v[32:35], v[152:155], v[196:199], v[32:35]
	v_mfma_f32_16x16x32_bf16 v[60:63], v[148:151], v[164:167], v[60:63]
	v_mfma_f32_16x16x32_bf16 v[56:59], v[156:159], v[164:167], v[56:59]
	v_mfma_f32_16x16x32_bf16 v[52:55], v[148:151], v[184:187], v[52:55]
	v_mfma_f32_16x16x32_bf16 v[48:51], v[156:159], v[184:187], v[48:51]
	v_mfma_f32_16x16x32_bf16 v[44:47], v[148:151], v[192:195], v[44:47]
	v_mfma_f32_16x16x32_bf16 v[40:43], v[156:159], v[192:195], v[40:43]
	v_mfma_f32_16x16x32_bf16 v[36:39], v[148:151], v[200:203], v[36:39]
	v_mfma_f32_16x16x32_bf16 v[32:35], v[156:159], v[200:203], v[32:35]
	s_barrier
	s_setprio 0
	s_add_u32 s52, s50, 0x8000
	s_addc_u32 s53, s51, 0
	s_mov_b32 m0, s69
	v_lshl_add_u64 v[208:209], s[52:53], 0, v[174:175]
	s_add_u32 s50, s50, 0xc000
	ds_read_b128 v[160:163], v251 offset:49152
	ds_read_b128 v[164:167], v251 offset:50176
	ds_read_b128 v[168:171], v251 offset:51200
	ds_read_b128 v[184:187], v251 offset:52224
	ds_read_b128 v[188:191], v251 offset:53248
	ds_read_b128 v[192:195], v251 offset:54272
	ds_read_b128 v[196:199], v251 offset:55296
	ds_read_b128 v[200:203], v251 offset:56320
	global_load_lds_dwordx4 v[208:209], off
	v_lshl_add_u64 v[208:209], s[52:53], 0, v[178:179]
	s_mov_b32 m0, s70
	s_addc_u32 s51, s51, 0
	global_load_lds_dwordx4 v[208:209], off
	v_lshl_add_u64 v[208:209], s[50:51], 0, v[174:175]
	s_mov_b32 m0, s74
	v_lshl_add_u64 v[204:205], v[204:205], 0, s[26:27]
	global_load_lds_dwordx4 v[208:209], off
	v_lshl_add_u64 v[208:209], s[50:51], 0, v[178:179]
	s_mov_b32 m0, s75
	s_nop 0
	global_load_lds_dwordx4 v[208:209], off
	s_mov_b32 m0, s71
	s_nop 0
	global_load_lds_dwordx4 v[204:205], off
	v_lshl_add_u64 v[204:205], v[206:207], 0, s[26:27]
	s_mov_b32 m0, s72
	s_nop 0
	global_load_lds_dwordx4 v[204:205], off
	s_waitcnt vmcnt(8)
	s_waitcnt lgkmcnt(0)
	s_setprio 1
	s_barrier
	v_mfma_f32_16x16x32_bf16 v[92:95], v[128:131], v[160:163], v[92:95]
	v_mfma_f32_16x16x32_bf16 v[88:91], v[136:139], v[160:163], v[88:91]
	v_mfma_f32_16x16x32_bf16 v[84:87], v[128:131], v[168:171], v[84:87]
	v_mfma_f32_16x16x32_bf16 v[80:83], v[136:139], v[168:171], v[80:83]
	v_mfma_f32_16x16x32_bf16 v[76:79], v[128:131], v[188:191], v[76:79]
	v_mfma_f32_16x16x32_bf16 v[72:75], v[136:139], v[188:191], v[72:75]
	v_mfma_f32_16x16x32_bf16 v[68:71], v[128:131], v[196:199], v[68:71]
	v_mfma_f32_16x16x32_bf16 v[64:67], v[136:139], v[196:199], v[64:67]
	v_mfma_f32_16x16x32_bf16 v[92:95], v[132:135], v[164:167], v[92:95]
	v_mfma_f32_16x16x32_bf16 v[88:91], v[140:143], v[164:167], v[88:91]
	v_mfma_f32_16x16x32_bf16 v[84:87], v[132:135], v[184:187], v[84:87]
	v_mfma_f32_16x16x32_bf16 v[80:83], v[140:143], v[184:187], v[80:83]
	v_mfma_f32_16x16x32_bf16 v[76:79], v[132:135], v[192:195], v[76:79]
	v_mfma_f32_16x16x32_bf16 v[72:75], v[140:143], v[192:195], v[72:75]
	v_mfma_f32_16x16x32_bf16 v[68:71], v[132:135], v[200:203], v[68:71]
	v_mfma_f32_16x16x32_bf16 v[64:67], v[140:143], v[200:203], v[64:67]
	v_mfma_f32_16x16x32_bf16 v[28:31], v[144:147], v[160:163], v[28:31]
	v_mfma_f32_16x16x32_bf16 v[24:27], v[152:155], v[160:163], v[24:27]
	v_mfma_f32_16x16x32_bf16 v[20:23], v[144:147], v[168:171], v[20:23]
	v_mfma_f32_16x16x32_bf16 v[16:19], v[152:155], v[168:171], v[16:19]
	v_mfma_f32_16x16x32_bf16 v[12:15], v[144:147], v[188:191], v[12:15]
	v_mfma_f32_16x16x32_bf16 v[8:11], v[152:155], v[188:191], v[8:11]
	v_mfma_f32_16x16x32_bf16 v[4:7], v[144:147], v[196:199], v[4:7]
	v_mfma_f32_16x16x32_bf16 v[0:3], v[152:155], v[196:199], v[0:3]
	v_mfma_f32_16x16x32_bf16 v[28:31], v[148:151], v[164:167], v[28:31]
	v_mfma_f32_16x16x32_bf16 v[24:27], v[156:159], v[164:167], v[24:27]
	v_mfma_f32_16x16x32_bf16 v[20:23], v[148:151], v[184:187], v[20:23]
	v_mfma_f32_16x16x32_bf16 v[16:19], v[156:159], v[184:187], v[16:19]
	v_mfma_f32_16x16x32_bf16 v[12:15], v[148:151], v[192:195], v[12:15]
	v_mfma_f32_16x16x32_bf16 v[8:11], v[156:159], v[192:195], v[8:11]
	v_mfma_f32_16x16x32_bf16 v[4:7], v[148:151], v[200:203], v[4:7]
	v_mfma_f32_16x16x32_bf16 v[0:3], v[156:159], v[200:203], v[0:3]
	s_barrier
	s_setprio 0
	s_add_i32 s80, s80, 2
	s_add_u32 s49, s49, 0x10000
	s_addc_u32 s55, s55, 0
	s_add_u32 s0, s0, 0x100
	s_addc_u32 s1, s1, 0
	s_cmp_gt_u32 s80, 29
.LBB0_1055:
	v_add_u32_e32 v140, s28, v215
	v_add_u32_e32 v156, s54, v215
	ds_read_b128 v[128:131], v140
	ds_read_b128 v[132:135], v140 offset:1024
	ds_read_b128 v[136:139], v140 offset:2048
	ds_read_b128 v[140:143], v140 offset:3072
	ds_read_b128 v[144:147], v156
	ds_read_b128 v[148:151], v156 offset:1024
	ds_read_b128 v[152:155], v156 offset:2048
	ds_read_b128 v[156:159], v156 offset:3072
	s_add_u32 s50, s0, 0xfff80080
	s_addc_u32 s51, s1, -1
	s_cmp_eq_u32 s80, 28
	s_cselect_b32 s53, s4, s51
	s_cselect_b32 s52, s5, s50
	s_cselect_b32 s51, s39, s55
	s_cselect_b32 s50, s41, s49
	v_lshl_add_u64 v[204:205], s[0:1], 0, v[180:181]
	s_add_i32 m0, s58, 0xc000
	ds_read_b128 v[160:163], v251
	ds_read_b128 v[164:167], v251 offset:1024
	ds_read_b128 v[168:171], v251 offset:2048
	ds_read_b128 v[184:187], v251 offset:3072
	ds_read_b128 v[188:191], v251 offset:4096
	ds_read_b128 v[192:195], v251 offset:5120
	ds_read_b128 v[196:199], v251 offset:6144
	ds_read_b128 v[200:203], v251 offset:7168
	global_load_lds_dwordx4 v[204:205], off
	v_lshl_add_u64 v[204:205], s[0:1], 0, v[182:183]
	s_add_i32 m0, s58, 0xe000
	s_nop 0
	global_load_lds_dwordx4 v[204:205], off
	s_waitcnt vmcnt(8)
	s_waitcnt lgkmcnt(0)
	s_setprio 1
	s_barrier
	v_mfma_f32_16x16x32_bf16 v[124:127], v[128:131], v[160:163], v[124:127]
	v_mfma_f32_16x16x32_bf16 v[120:123], v[136:139], v[160:163], v[120:123]
	v_mfma_f32_16x16x32_bf16 v[116:119], v[128:131], v[168:171], v[116:119]
	v_mfma_f32_16x16x32_bf16 v[112:115], v[136:139], v[168:171], v[112:115]
	v_mfma_f32_16x16x32_bf16 v[108:111], v[128:131], v[188:191], v[108:111]
	v_mfma_f32_16x16x32_bf16 v[104:107], v[136:139], v[188:191], v[104:107]
	v_mfma_f32_16x16x32_bf16 v[100:103], v[128:131], v[196:199], v[100:103]
	v_mfma_f32_16x16x32_bf16 v[96:99], v[136:139], v[196:199], v[96:99]
	v_mfma_f32_16x16x32_bf16 v[124:127], v[132:135], v[164:167], v[124:127]
	v_mfma_f32_16x16x32_bf16 v[120:123], v[140:143], v[164:167], v[120:123]
	v_mfma_f32_16x16x32_bf16 v[116:119], v[132:135], v[184:187], v[116:119]
	v_mfma_f32_16x16x32_bf16 v[112:115], v[140:143], v[184:187], v[112:115]
	v_mfma_f32_16x16x32_bf16 v[108:111], v[132:135], v[192:195], v[108:111]
	v_mfma_f32_16x16x32_bf16 v[104:107], v[140:143], v[192:195], v[104:107]
	v_mfma_f32_16x16x32_bf16 v[100:103], v[132:135], v[200:203], v[100:103]
	v_mfma_f32_16x16x32_bf16 v[96:99], v[140:143], v[200:203], v[96:99]
	v_mfma_f32_16x16x32_bf16 v[60:63], v[144:147], v[160:163], v[60:63]
	v_mfma_f32_16x16x32_bf16 v[56:59], v[152:155], v[160:163], v[56:59]
	v_mfma_f32_16x16x32_bf16 v[52:55], v[144:147], v[168:171], v[52:55]
	v_mfma_f32_16x16x32_bf16 v[48:51], v[152:155], v[168:171], v[48:51]
	v_mfma_f32_16x16x32_bf16 v[44:47], v[144:147], v[188:191], v[44:47]
	v_mfma_f32_16x16x32_bf16 v[40:43], v[152:155], v[188:191], v[40:43]
	v_mfma_f32_16x16x32_bf16 v[36:39], v[144:147], v[196:199], v[36:39]
	v_mfma_f32_16x16x32_bf16 v[32:35], v[152:155], v[196:199], v[32:35]
	v_mfma_f32_16x16x32_bf16 v[60:63], v[148:151], v[164:167], v[60:63]
	v_mfma_f32_16x16x32_bf16 v[56:59], v[156:159], v[164:167], v[56:59]
	v_mfma_f32_16x16x32_bf16 v[52:55], v[148:151], v[184:187], v[52:55]
	v_mfma_f32_16x16x32_bf16 v[48:51], v[156:159], v[184:187], v[48:51]
	v_mfma_f32_16x16x32_bf16 v[44:47], v[148:151], v[192:195], v[44:47]
	v_mfma_f32_16x16x32_bf16 v[40:43], v[156:159], v[192:195], v[40:43]
	v_mfma_f32_16x16x32_bf16 v[36:39], v[148:151], v[200:203], v[36:39]
	v_mfma_f32_16x16x32_bf16 v[32:35], v[156:159], v[200:203], v[32:35]
	s_barrier
	s_setprio 0
	s_mov_b32 m0, s30
	v_lshl_add_u64 v[204:205], s[50:51], 0, v[174:175]
	s_add_u32 s82, s50, 0x4000
	ds_read_b128 v[160:163], v251 offset:16384
	ds_read_b128 v[164:167], v251 offset:17408
	ds_read_b128 v[168:171], v251 offset:18432
	ds_read_b128 v[184:187], v251 offset:19456
	ds_read_b128 v[188:191], v251 offset:20480
	ds_read_b128 v[192:195], v251 offset:21504
	ds_read_b128 v[196:199], v251 offset:22528
	ds_read_b128 v[200:203], v251 offset:23552
	global_load_lds_dwordx4 v[204:205], off
	v_lshl_add_u64 v[204:205], s[50:51], 0, v[178:179]
	s_mov_b32 m0, s43
	s_addc_u32 s83, s51, 0
	global_load_lds_dwordx4 v[204:205], off
	v_lshl_add_u64 v[204:205], s[82:83], 0, v[174:175]
	s_mov_b32 m0, s56
	v_lshl_add_u64 v[206:207], s[52:53], 0, v[176:177]
	global_load_lds_dwordx4 v[204:205], off
	v_lshl_add_u64 v[204:205], s[82:83], 0, v[178:179]
	s_mov_b32 m0, s57
	s_nop 0
	global_load_lds_dwordx4 v[204:205], off
	v_lshl_add_u64 v[204:205], s[52:53], 0, v[172:173]
	s_mov_b32 m0, s58
	s_nop 0
	global_load_lds_dwordx4 v[204:205], off
	s_mov_b32 m0, s59
	s_nop 0
	global_load_lds_dwordx4 v[206:207], off
	s_waitcnt vmcnt(8)
	s_waitcnt lgkmcnt(0)
	s_setprio 1
	s_barrier
	v_mfma_f32_16x16x32_bf16 v[92:95], v[128:131], v[160:163], v[92:95]
	v_mfma_f32_16x16x32_bf16 v[88:91], v[136:139], v[160:163], v[88:91]
	v_mfma_f32_16x16x32_bf16 v[84:87], v[128:131], v[168:171], v[84:87]
	v_mfma_f32_16x16x32_bf16 v[80:83], v[136:139], v[168:171], v[80:83]
	v_mfma_f32_16x16x32_bf16 v[76:79], v[128:131], v[188:191], v[76:79]
	v_mfma_f32_16x16x32_bf16 v[72:75], v[136:139], v[188:191], v[72:75]
	v_mfma_f32_16x16x32_bf16 v[68:71], v[128:131], v[196:199], v[68:71]
	v_mfma_f32_16x16x32_bf16 v[64:67], v[136:139], v[196:199], v[64:67]
	v_mfma_f32_16x16x32_bf16 v[92:95], v[132:135], v[164:167], v[92:95]
	v_mfma_f32_16x16x32_bf16 v[88:91], v[140:143], v[164:167], v[88:91]
	v_mfma_f32_16x16x32_bf16 v[84:87], v[132:135], v[184:187], v[84:87]
	v_mfma_f32_16x16x32_bf16 v[80:83], v[140:143], v[184:187], v[80:83]
	v_mfma_f32_16x16x32_bf16 v[76:79], v[132:135], v[192:195], v[76:79]
	v_mfma_f32_16x16x32_bf16 v[72:75], v[140:143], v[192:195], v[72:75]
	v_mfma_f32_16x16x32_bf16 v[68:71], v[132:135], v[200:203], v[68:71]
	v_mfma_f32_16x16x32_bf16 v[64:67], v[140:143], v[200:203], v[64:67]
	v_mfma_f32_16x16x32_bf16 v[28:31], v[144:147], v[160:163], v[28:31]
	v_mfma_f32_16x16x32_bf16 v[24:27], v[152:155], v[160:163], v[24:27]
	v_mfma_f32_16x16x32_bf16 v[20:23], v[144:147], v[168:171], v[20:23]
	v_mfma_f32_16x16x32_bf16 v[16:19], v[152:155], v[168:171], v[16:19]
	v_mfma_f32_16x16x32_bf16 v[12:15], v[144:147], v[188:191], v[12:15]
	v_mfma_f32_16x16x32_bf16 v[8:11], v[152:155], v[188:191], v[8:11]
	v_mfma_f32_16x16x32_bf16 v[4:7], v[144:147], v[196:199], v[4:7]
	v_mfma_f32_16x16x32_bf16 v[0:3], v[152:155], v[196:199], v[0:3]
	v_mfma_f32_16x16x32_bf16 v[28:31], v[148:151], v[164:167], v[28:31]
	v_mfma_f32_16x16x32_bf16 v[24:27], v[156:159], v[164:167], v[24:27]
	v_mfma_f32_16x16x32_bf16 v[20:23], v[148:151], v[184:187], v[20:23]
	v_mfma_f32_16x16x32_bf16 v[16:19], v[156:159], v[184:187], v[16:19]
	v_mfma_f32_16x16x32_bf16 v[12:15], v[148:151], v[192:195], v[12:15]
	v_mfma_f32_16x16x32_bf16 v[8:11], v[156:159], v[192:195], v[8:11]
	v_mfma_f32_16x16x32_bf16 v[4:7], v[148:151], v[200:203], v[4:7]
	v_mfma_f32_16x16x32_bf16 v[0:3], v[156:159], v[200:203], v[0:3]
	s_barrier
	s_setprio 0
	v_add_u32_e32 v140, s68, v215
	v_add_u32_e32 v156, s73, v215
	ds_read_b128 v[128:131], v140
	ds_read_b128 v[132:135], v140 offset:1024
	ds_read_b128 v[136:139], v140 offset:2048
	ds_read_b128 v[140:143], v140 offset:3072
	ds_read_b128 v[144:147], v156
	ds_read_b128 v[148:151], v156 offset:1024
	ds_read_b128 v[152:155], v156 offset:2048
	ds_read_b128 v[156:159], v156 offset:3072
	s_add_u32 s52, s52, 0x80000
	s_addc_u32 s53, s53, 0
	s_mov_b32 m0, s60
	v_lshl_add_u64 v[208:209], s[52:53], 0, v[172:173]
	ds_read_b128 v[160:163], v251 offset:32768
	ds_read_b128 v[164:167], v251 offset:33792
	ds_read_b128 v[168:171], v251 offset:34816
	ds_read_b128 v[184:187], v251 offset:35840
	ds_read_b128 v[188:191], v251 offset:36864
	ds_read_b128 v[192:195], v251 offset:37888
	ds_read_b128 v[196:199], v251 offset:38912
	ds_read_b128 v[200:203], v251 offset:39936
	global_load_lds_dwordx4 v[208:209], off
	v_lshl_add_u64 v[208:209], s[52:53], 0, v[176:177]
	s_mov_b32 m0, s61
	s_nop 0
	global_load_lds_dwordx4 v[208:209], off
	s_waitcnt vmcnt(8)
	s_waitcnt lgkmcnt(0)
	s_setprio 1
	s_barrier
	v_mfma_f32_16x16x32_bf16 v[124:127], v[128:131], v[160:163], v[124:127]
	v_mfma_f32_16x16x32_bf16 v[120:123], v[136:139], v[160:163], v[120:123]
	v_mfma_f32_16x16x32_bf16 v[116:119], v[128:131], v[168:171], v[116:119]
	v_mfma_f32_16x16x32_bf16 v[112:115], v[136:139], v[168:171], v[112:115]
	v_mfma_f32_16x16x32_bf16 v[108:111], v[128:131], v[188:191], v[108:111]
	v_mfma_f32_16x16x32_bf16 v[104:107], v[136:139], v[188:191], v[104:107]
	v_mfma_f32_16x16x32_bf16 v[100:103], v[128:131], v[196:199], v[100:103]
	v_mfma_f32_16x16x32_bf16 v[96:99], v[136:139], v[196:199], v[96:99]
	v_mfma_f32_16x16x32_bf16 v[124:127], v[132:135], v[164:167], v[124:127]
	v_mfma_f32_16x16x32_bf16 v[120:123], v[140:143], v[164:167], v[120:123]
	v_mfma_f32_16x16x32_bf16 v[116:119], v[132:135], v[184:187], v[116:119]
	v_mfma_f32_16x16x32_bf16 v[112:115], v[140:143], v[184:187], v[112:115]
	v_mfma_f32_16x16x32_bf16 v[108:111], v[132:135], v[192:195], v[108:111]
	v_mfma_f32_16x16x32_bf16 v[104:107], v[140:143], v[192:195], v[104:107]
	v_mfma_f32_16x16x32_bf16 v[100:103], v[132:135], v[200:203], v[100:103]
	v_mfma_f32_16x16x32_bf16 v[96:99], v[140:143], v[200:203], v[96:99]
	v_mfma_f32_16x16x32_bf16 v[60:63], v[144:147], v[160:163], v[60:63]
	v_mfma_f32_16x16x32_bf16 v[56:59], v[152:155], v[160:163], v[56:59]
	v_mfma_f32_16x16x32_bf16 v[52:55], v[144:147], v[168:171], v[52:55]
	v_mfma_f32_16x16x32_bf16 v[48:51], v[152:155], v[168:171], v[48:51]
	v_mfma_f32_16x16x32_bf16 v[44:47], v[144:147], v[188:191], v[44:47]
	v_mfma_f32_16x16x32_bf16 v[40:43], v[152:155], v[188:191], v[40:43]
	v_mfma_f32_16x16x32_bf16 v[36:39], v[144:147], v[196:199], v[36:39]
	v_mfma_f32_16x16x32_bf16 v[32:35], v[152:155], v[196:199], v[32:35]
	v_mfma_f32_16x16x32_bf16 v[60:63], v[148:151], v[164:167], v[60:63]
	v_mfma_f32_16x16x32_bf16 v[56:59], v[156:159], v[164:167], v[56:59]
	v_mfma_f32_16x16x32_bf16 v[52:55], v[148:151], v[184:187], v[52:55]
	v_mfma_f32_16x16x32_bf16 v[48:51], v[156:159], v[184:187], v[48:51]
	v_mfma_f32_16x16x32_bf16 v[44:47], v[148:151], v[192:195], v[44:47]
	v_mfma_f32_16x16x32_bf16 v[40:43], v[156:159], v[192:195], v[40:43]
	v_mfma_f32_16x16x32_bf16 v[36:39], v[148:151], v[200:203], v[36:39]
	v_mfma_f32_16x16x32_bf16 v[32:35], v[156:159], v[200:203], v[32:35]
	s_barrier
	s_setprio 0
	s_add_u32 s52, s50, 0x8000
	s_addc_u32 s53, s51, 0
	s_mov_b32 m0, s69
	v_lshl_add_u64 v[208:209], s[52:53], 0, v[174:175]
	s_add_u32 s50, s50, 0xc000
	ds_read_b128 v[160:163], v251 offset:49152
	ds_read_b128 v[164:167], v251 offset:50176
	ds_read_b128 v[168:171], v251 offset:51200
	ds_read_b128 v[184:187], v251 offset:52224
	ds_read_b128 v[188:191], v251 offset:53248
	ds_read_b128 v[192:195], v251 offset:54272
	ds_read_b128 v[196:199], v251 offset:55296
	ds_read_b128 v[200:203], v251 offset:56320
	global_load_lds_dwordx4 v[208:209], off
	v_lshl_add_u64 v[208:209], s[52:53], 0, v[178:179]
	s_mov_b32 m0, s70
	s_addc_u32 s51, s51, 0
	global_load_lds_dwordx4 v[208:209], off
	v_lshl_add_u64 v[208:209], s[50:51], 0, v[174:175]
	s_mov_b32 m0, s74
	v_lshl_add_u64 v[204:205], v[204:205], 0, s[26:27]
	global_load_lds_dwordx4 v[208:209], off
	v_lshl_add_u64 v[208:209], s[50:51], 0, v[178:179]
	s_mov_b32 m0, s75
	s_nop 0
	global_load_lds_dwordx4 v[208:209], off
	s_mov_b32 m0, s71
	s_nop 0
	global_load_lds_dwordx4 v[204:205], off
	v_lshl_add_u64 v[204:205], v[206:207], 0, s[26:27]
	s_mov_b32 m0, s72
	s_nop 0
	global_load_lds_dwordx4 v[204:205], off
	s_waitcnt vmcnt(8)
	s_waitcnt lgkmcnt(0)
	s_setprio 1
	s_barrier
	v_mfma_f32_16x16x32_bf16 v[92:95], v[128:131], v[160:163], v[92:95]
	v_mfma_f32_16x16x32_bf16 v[88:91], v[136:139], v[160:163], v[88:91]
	v_mfma_f32_16x16x32_bf16 v[84:87], v[128:131], v[168:171], v[84:87]
	v_mfma_f32_16x16x32_bf16 v[80:83], v[136:139], v[168:171], v[80:83]
	v_mfma_f32_16x16x32_bf16 v[76:79], v[128:131], v[188:191], v[76:79]
	v_mfma_f32_16x16x32_bf16 v[72:75], v[136:139], v[188:191], v[72:75]
	v_mfma_f32_16x16x32_bf16 v[68:71], v[128:131], v[196:199], v[68:71]
	v_mfma_f32_16x16x32_bf16 v[64:67], v[136:139], v[196:199], v[64:67]
	v_mfma_f32_16x16x32_bf16 v[92:95], v[132:135], v[164:167], v[92:95]
	v_mfma_f32_16x16x32_bf16 v[88:91], v[140:143], v[164:167], v[88:91]
	v_mfma_f32_16x16x32_bf16 v[84:87], v[132:135], v[184:187], v[84:87]
	v_mfma_f32_16x16x32_bf16 v[80:83], v[140:143], v[184:187], v[80:83]
	v_mfma_f32_16x16x32_bf16 v[76:79], v[132:135], v[192:195], v[76:79]
	v_mfma_f32_16x16x32_bf16 v[72:75], v[140:143], v[192:195], v[72:75]
	v_mfma_f32_16x16x32_bf16 v[68:71], v[132:135], v[200:203], v[68:71]
	v_mfma_f32_16x16x32_bf16 v[64:67], v[140:143], v[200:203], v[64:67]
	v_mfma_f32_16x16x32_bf16 v[28:31], v[144:147], v[160:163], v[28:31]
	v_mfma_f32_16x16x32_bf16 v[24:27], v[152:155], v[160:163], v[24:27]
	v_mfma_f32_16x16x32_bf16 v[20:23], v[144:147], v[168:171], v[20:23]
	v_mfma_f32_16x16x32_bf16 v[16:19], v[152:155], v[168:171], v[16:19]
	v_mfma_f32_16x16x32_bf16 v[12:15], v[144:147], v[188:191], v[12:15]
	v_mfma_f32_16x16x32_bf16 v[8:11], v[152:155], v[188:191], v[8:11]
	v_mfma_f32_16x16x32_bf16 v[4:7], v[144:147], v[196:199], v[4:7]
	v_mfma_f32_16x16x32_bf16 v[0:3], v[152:155], v[196:199], v[0:3]
	v_mfma_f32_16x16x32_bf16 v[28:31], v[148:151], v[164:167], v[28:31]
	v_mfma_f32_16x16x32_bf16 v[24:27], v[156:159], v[164:167], v[24:27]
	v_mfma_f32_16x16x32_bf16 v[20:23], v[148:151], v[184:187], v[20:23]
	v_mfma_f32_16x16x32_bf16 v[16:19], v[156:159], v[184:187], v[16:19]
	v_mfma_f32_16x16x32_bf16 v[12:15], v[148:151], v[192:195], v[12:15]
	v_mfma_f32_16x16x32_bf16 v[8:11], v[156:159], v[192:195], v[8:11]
	v_mfma_f32_16x16x32_bf16 v[4:7], v[148:151], v[200:203], v[4:7]
	v_mfma_f32_16x16x32_bf16 v[0:3], v[156:159], v[200:203], v[0:3]
	s_barrier
	s_setprio 0
	s_add_i32 s80, s80, 2
	s_add_u32 s49, s49, 0x10000
	s_addc_u32 s55, s55, 0
	s_add_u32 s0, s0, 0x100
	s_addc_u32 s1, s1, 0
	s_cmp_gt_u32 s80, 29
	s_cbranch_scc0 .LBB0_1055
	v_mov_b64_e32 v[220:221], 0x1ff
	v_mov_b64_e32 v[218:219], 0x200
	s_and_b64 vcc, exec, s[34:35]
	s_cbranch_vccz .LBB0_1058
	s_barrier

.LBB0_1172:
	s_ashr_i32 s39, s38, 31
	s_lshl_b64 s[4:5], s[38:39], 20
	s_add_u32 s40, s18, s4
	s_addc_u32 s41, s19, s5
	s_and_b64 s[4:5], s[36:37], exec
	s_cselect_b32 s4, s41, s1
	s_cselect_b32 s5, s40, s0
	s_ashr_i32 s35, s34, 31
	s_lshl_b64 s[42:43], s[34:35], 20
	s_add_u32 s42, s16, s42
	s_addc_u32 s43, s17, s43
	s_and_b64 s[48:49], s[36:37], exec
	s_cselect_b32 s35, s43, s47
	s_cselect_b32 s39, s42, s46
	s_add_u32 s76, s46, 0x10000
	s_addc_u32 s77, s47, 0
	s_mov_b32 s78, -2
	v_add_u32_e32 v124, s28, v156
	v_add_u32_e32 v170, s45, v156
	ds_read_b128 v[108:111], v124
	ds_read_b128 v[112:115], v124 offset:1024
	ds_read_b128 v[120:123], v124 offset:2048
	ds_read_b128 v[124:127], v124 offset:3072
	ds_read_b128 v[158:161], v170
	ds_read_b128 v[162:165], v170 offset:1024
	ds_read_b128 v[166:169], v170 offset:2048
	ds_read_b128 v[170:173], v170 offset:3072
	s_add_u32 s46, s0, 0x10000
	s_addc_u32 s47, s1, 0
	s_cmp_eq_u32 s78, 28
	s_cselect_b32 s52, s5, s46
	s_cselect_b32 s53, s4, s47
	s_cselect_b32 s50, s39, s76
	s_cselect_b32 s51, s35, s77
	s_add_u32 s48, s52, 0x8000
	s_addc_u32 s49, s53, 0
	v_lshl_add_u64 v[206:207], s[0:1], 0, v[152:153]
	s_add_i32 m0, s56, 0xc000
	ds_read_b128 v[174:177], v157
	ds_read_b128 v[178:181], v157 offset:1024
	ds_read_b128 v[182:185], v157 offset:2048
	ds_read_b128 v[186:189], v157 offset:3072
	ds_read_b128 v[190:193], v157 offset:4096
	ds_read_b128 v[194:197], v157 offset:5120
	ds_read_b128 v[198:201], v157 offset:6144
	ds_read_b128 v[202:205], v157 offset:7168
	global_load_lds_dwordx4 v[206:207], off
	v_lshl_add_u64 v[206:207], s[0:1], 0, v[154:155]
	s_add_i32 m0, s56, 0xe000
	s_nop 0
	global_load_lds_dwordx4 v[206:207], off
	s_waitcnt vmcnt(8)
	s_waitcnt lgkmcnt(0)
	s_setprio 1
	s_barrier
	v_mfma_f32_16x16x32_bf16 v[140:143], v[108:111], v[174:177], 0
	v_mfma_f32_16x16x32_bf16 v[136:139], v[120:123], v[174:177], 0
	v_mfma_f32_16x16x32_bf16 v[116:119], v[108:111], v[182:185], 0
	v_mfma_f32_16x16x32_bf16 v[104:107], v[120:123], v[182:185], 0
	v_mfma_f32_16x16x32_bf16 v[92:95], v[108:111], v[190:193], 0
	v_mfma_f32_16x16x32_bf16 v[88:91], v[120:123], v[190:193], 0
	v_mfma_f32_16x16x32_bf16 v[76:79], v[108:111], v[198:201], 0
	v_mfma_f32_16x16x32_bf16 v[72:75], v[120:123], v[198:201], 0
	v_mfma_f32_16x16x32_bf16 v[140:143], v[112:115], v[178:181], v[140:143]
	v_mfma_f32_16x16x32_bf16 v[136:139], v[124:127], v[178:181], v[136:139]
	v_mfma_f32_16x16x32_bf16 v[116:119], v[112:115], v[186:189], v[116:119]
	v_mfma_f32_16x16x32_bf16 v[104:107], v[124:127], v[186:189], v[104:107]
	v_mfma_f32_16x16x32_bf16 v[92:95], v[112:115], v[194:197], v[92:95]
	v_mfma_f32_16x16x32_bf16 v[88:91], v[124:127], v[194:197], v[88:91]
	v_mfma_f32_16x16x32_bf16 v[76:79], v[112:115], v[202:205], v[76:79]
	v_mfma_f32_16x16x32_bf16 v[72:75], v[124:127], v[202:205], v[72:75]
	v_mfma_f32_16x16x32_bf16 v[132:135], v[158:161], v[174:177], 0
	v_mfma_f32_16x16x32_bf16 v[128:131], v[166:169], v[174:177], 0
	v_mfma_f32_16x16x32_bf16 v[100:103], v[158:161], v[182:185], 0
	v_mfma_f32_16x16x32_bf16 v[96:99], v[166:169], v[182:185], 0
	v_mfma_f32_16x16x32_bf16 v[84:87], v[158:161], v[190:193], 0
	v_mfma_f32_16x16x32_bf16 v[80:83], v[166:169], v[190:193], 0
	v_mfma_f32_16x16x32_bf16 v[68:71], v[158:161], v[198:201], 0
	v_mfma_f32_16x16x32_bf16 v[64:67], v[166:169], v[198:201], 0
	v_mfma_f32_16x16x32_bf16 v[132:135], v[162:165], v[178:181], v[132:135]
	v_mfma_f32_16x16x32_bf16 v[128:131], v[170:173], v[178:181], v[128:131]
	v_mfma_f32_16x16x32_bf16 v[100:103], v[162:165], v[186:189], v[100:103]
	v_mfma_f32_16x16x32_bf16 v[96:99], v[170:173], v[186:189], v[96:99]
	v_mfma_f32_16x16x32_bf16 v[84:87], v[162:165], v[194:197], v[84:87]
	v_mfma_f32_16x16x32_bf16 v[80:83], v[170:173], v[194:197], v[80:83]
	v_mfma_f32_16x16x32_bf16 v[68:71], v[162:165], v[202:205], v[68:71]
	v_mfma_f32_16x16x32_bf16 v[64:67], v[170:173], v[202:205], v[64:67]
	s_barrier
	s_setprio 0
	s_mov_b32 m0, s30
	v_lshl_add_u64 v[206:207], s[50:51], 0, v[146:147]
	s_add_u32 s0, s50, 0x4000
	ds_read_b128 v[174:177], v157 offset:16384
	ds_read_b128 v[178:181], v157 offset:17408
	ds_read_b128 v[182:185], v157 offset:18432
	ds_read_b128 v[186:189], v157 offset:19456
	ds_read_b128 v[190:193], v157 offset:20480
	ds_read_b128 v[194:197], v157 offset:21504
	ds_read_b128 v[198:201], v157 offset:22528
	ds_read_b128 v[202:205], v157 offset:23552
	global_load_lds_dwordx4 v[206:207], off
	v_lshl_add_u64 v[206:207], s[50:51], 0, v[150:151]
	s_mov_b32 m0, s31
	s_addc_u32 s1, s51, 0
	global_load_lds_dwordx4 v[206:207], off
	v_lshl_add_u64 v[206:207], s[0:1], 0, v[146:147]
	s_mov_b32 m0, s54
	s_nop 0
	global_load_lds_dwordx4 v[206:207], off
	v_lshl_add_u64 v[206:207], s[0:1], 0, v[150:151]
	s_mov_b32 m0, s55
	s_nop 0
	global_load_lds_dwordx4 v[206:207], off
	v_lshl_add_u64 v[206:207], s[52:53], 0, v[144:145]
	s_mov_b32 m0, s56
	s_nop 0
	global_load_lds_dwordx4 v[206:207], off
	v_lshl_add_u64 v[206:207], s[52:53], 0, v[148:149]
	s_mov_b32 m0, s57
	s_nop 0
	global_load_lds_dwordx4 v[206:207], off
	s_waitcnt vmcnt(8)
	s_waitcnt lgkmcnt(0)
	s_setprio 1
	s_barrier
	v_mfma_f32_16x16x32_bf16 v[60:63], v[108:111], v[174:177], 0
	v_mfma_f32_16x16x32_bf16 v[56:59], v[120:123], v[174:177], 0
	v_mfma_f32_16x16x32_bf16 v[44:47], v[108:111], v[182:185], 0
	v_mfma_f32_16x16x32_bf16 v[40:43], v[120:123], v[182:185], 0
	v_mfma_f32_16x16x32_bf16 v[28:31], v[108:111], v[190:193], 0
	v_mfma_f32_16x16x32_bf16 v[24:27], v[120:123], v[190:193], 0
	v_mfma_f32_16x16x32_bf16 v[12:15], v[108:111], v[198:201], 0
	v_mfma_f32_16x16x32_bf16 v[8:11], v[120:123], v[198:201], 0
	v_mfma_f32_16x16x32_bf16 v[60:63], v[112:115], v[178:181], v[60:63]
	v_mfma_f32_16x16x32_bf16 v[56:59], v[124:127], v[178:181], v[56:59]
	v_mfma_f32_16x16x32_bf16 v[44:47], v[112:115], v[186:189], v[44:47]
	v_mfma_f32_16x16x32_bf16 v[40:43], v[124:127], v[186:189], v[40:43]
	v_mfma_f32_16x16x32_bf16 v[28:31], v[112:115], v[194:197], v[28:31]
	v_mfma_f32_16x16x32_bf16 v[24:27], v[124:127], v[194:197], v[24:27]
	v_mfma_f32_16x16x32_bf16 v[12:15], v[112:115], v[202:205], v[12:15]
	v_mfma_f32_16x16x32_bf16 v[8:11], v[124:127], v[202:205], v[8:11]
	v_mfma_f32_16x16x32_bf16 v[52:55], v[158:161], v[174:177], 0
	v_mfma_f32_16x16x32_bf16 v[48:51], v[166:169], v[174:177], 0
	v_mfma_f32_16x16x32_bf16 v[36:39], v[158:161], v[182:185], 0
	v_mfma_f32_16x16x32_bf16 v[32:35], v[166:169], v[182:185], 0
	v_mfma_f32_16x16x32_bf16 v[20:23], v[158:161], v[190:193], 0
	v_mfma_f32_16x16x32_bf16 v[16:19], v[166:169], v[190:193], 0
	v_mfma_f32_16x16x32_bf16 v[4:7], v[158:161], v[198:201], 0
	v_mfma_f32_16x16x32_bf16 v[0:3], v[166:169], v[198:201], 0
	v_mfma_f32_16x16x32_bf16 v[52:55], v[162:165], v[178:181], v[52:55]
	v_mfma_f32_16x16x32_bf16 v[48:51], v[170:173], v[178:181], v[48:51]
	v_mfma_f32_16x16x32_bf16 v[36:39], v[162:165], v[186:189], v[36:39]
	v_mfma_f32_16x16x32_bf16 v[32:35], v[170:173], v[186:189], v[32:35]
	v_mfma_f32_16x16x32_bf16 v[20:23], v[162:165], v[194:197], v[20:23]
	v_mfma_f32_16x16x32_bf16 v[16:19], v[170:173], v[194:197], v[16:19]
	v_mfma_f32_16x16x32_bf16 v[4:7], v[162:165], v[202:205], v[4:7]
	v_mfma_f32_16x16x32_bf16 v[0:3], v[170:173], v[202:205], v[0:3]
	s_barrier
	s_setprio 0
	v_add_u32_e32 v124, s62, v156
	v_add_u32_e32 v170, s67, v156
	ds_read_b128 v[108:111], v124
	ds_read_b128 v[112:115], v124 offset:1024
	ds_read_b128 v[120:123], v124 offset:2048
	ds_read_b128 v[124:127], v124 offset:3072
	ds_read_b128 v[158:161], v170
	ds_read_b128 v[162:165], v170 offset:1024
	ds_read_b128 v[166:169], v170 offset:2048
	ds_read_b128 v[170:173], v170 offset:3072
	s_add_u32 s0, s52, 0x4000
	s_addc_u32 s1, s53, 0
	s_mov_b32 m0, s58
	v_lshl_add_u64 v[206:207], s[0:1], 0, v[144:145]
	ds_read_b128 v[174:177], v157 offset:32768
	ds_read_b128 v[178:181], v157 offset:33792
	ds_read_b128 v[182:185], v157 offset:34816
	ds_read_b128 v[186:189], v157 offset:35840
	ds_read_b128 v[190:193], v157 offset:36864
	ds_read_b128 v[194:197], v157 offset:37888
	ds_read_b128 v[198:201], v157 offset:38912
	ds_read_b128 v[202:205], v157 offset:39936
	global_load_lds_dwordx4 v[206:207], off
	v_lshl_add_u64 v[206:207], s[0:1], 0, v[148:149]
	s_mov_b32 m0, s59
	s_nop 0
	global_load_lds_dwordx4 v[206:207], off
	s_waitcnt vmcnt(8)
	s_waitcnt lgkmcnt(0)
	s_setprio 1
	s_barrier
	v_mfma_f32_16x16x32_bf16 v[140:143], v[108:111], v[174:177], v[140:143]
	v_mfma_f32_16x16x32_bf16 v[136:139], v[120:123], v[174:177], v[136:139]
	v_mfma_f32_16x16x32_bf16 v[116:119], v[108:111], v[182:185], v[116:119]
	v_mfma_f32_16x16x32_bf16 v[104:107], v[120:123], v[182:185], v[104:107]
	v_mfma_f32_16x16x32_bf16 v[92:95], v[108:111], v[190:193], v[92:95]
	v_mfma_f32_16x16x32_bf16 v[88:91], v[120:123], v[190:193], v[88:91]
	v_mfma_f32_16x16x32_bf16 v[76:79], v[108:111], v[198:201], v[76:79]
	v_mfma_f32_16x16x32_bf16 v[72:75], v[120:123], v[198:201], v[72:75]
	v_mfma_f32_16x16x32_bf16 v[140:143], v[112:115], v[178:181], v[140:143]
	v_mfma_f32_16x16x32_bf16 v[136:139], v[124:127], v[178:181], v[136:139]
	v_mfma_f32_16x16x32_bf16 v[116:119], v[112:115], v[186:189], v[116:119]
	v_mfma_f32_16x16x32_bf16 v[104:107], v[124:127], v[186:189], v[104:107]
	v_mfma_f32_16x16x32_bf16 v[92:95], v[112:115], v[194:197], v[92:95]
	v_mfma_f32_16x16x32_bf16 v[88:91], v[124:127], v[194:197], v[88:91]
	v_mfma_f32_16x16x32_bf16 v[76:79], v[112:115], v[202:205], v[76:79]
	v_mfma_f32_16x16x32_bf16 v[72:75], v[124:127], v[202:205], v[72:75]
	v_mfma_f32_16x16x32_bf16 v[132:135], v[158:161], v[174:177], v[132:135]
	v_mfma_f32_16x16x32_bf16 v[128:131], v[166:169], v[174:177], v[128:131]
	v_mfma_f32_16x16x32_bf16 v[100:103], v[158:161], v[182:185], v[100:103]
	v_mfma_f32_16x16x32_bf16 v[96:99], v[166:169], v[182:185], v[96:99]
	v_mfma_f32_16x16x32_bf16 v[84:87], v[158:161], v[190:193], v[84:87]
	v_mfma_f32_16x16x32_bf16 v[80:83], v[166:169], v[190:193], v[80:83]
	v_mfma_f32_16x16x32_bf16 v[68:71], v[158:161], v[198:201], v[68:71]
	v_mfma_f32_16x16x32_bf16 v[64:67], v[166:169], v[198:201], v[64:67]
	v_mfma_f32_16x16x32_bf16 v[132:135], v[162:165], v[178:181], v[132:135]
	v_mfma_f32_16x16x32_bf16 v[128:131], v[170:173], v[178:181], v[128:131]
	v_mfma_f32_16x16x32_bf16 v[100:103], v[162:165], v[186:189], v[100:103]
	v_mfma_f32_16x16x32_bf16 v[96:99], v[170:173], v[186:189], v[96:99]
	v_mfma_f32_16x16x32_bf16 v[84:87], v[162:165], v[194:197], v[84:87]
	v_mfma_f32_16x16x32_bf16 v[80:83], v[170:173], v[194:197], v[80:83]
	v_mfma_f32_16x16x32_bf16 v[68:71], v[162:165], v[202:205], v[68:71]
	v_mfma_f32_16x16x32_bf16 v[64:67], v[170:173], v[202:205], v[64:67]
	s_barrier
	s_setprio 0
	s_add_u32 s0, s50, 0x8000
	s_addc_u32 s1, s51, 0
	s_mov_b32 m0, s63
	v_lshl_add_u64 v[206:207], s[0:1], 0, v[146:147]
	ds_read_b128 v[174:177], v157 offset:49152
	ds_read_b128 v[178:181], v157 offset:50176
	ds_read_b128 v[182:185], v157 offset:51200
	ds_read_b128 v[186:189], v157 offset:52224
	ds_read_b128 v[190:193], v157 offset:53248
	ds_read_b128 v[194:197], v157 offset:54272
	ds_read_b128 v[198:201], v157 offset:55296
	ds_read_b128 v[202:205], v157 offset:56320
	global_load_lds_dwordx4 v[206:207], off
	v_lshl_add_u64 v[206:207], s[0:1], 0, v[150:151]
	s_add_u32 s0, s50, 0xc000
	s_mov_b32 m0, s64
	s_addc_u32 s1, s51, 0
	global_load_lds_dwordx4 v[206:207], off
	v_lshl_add_u64 v[206:207], s[0:1], 0, v[146:147]
	s_mov_b32 m0, s68
	s_nop 0
	global_load_lds_dwordx4 v[206:207], off
	v_lshl_add_u64 v[206:207], s[0:1], 0, v[150:151]
	s_mov_b32 m0, s69
	s_nop 0
	global_load_lds_dwordx4 v[206:207], off
	v_lshl_add_u64 v[206:207], s[48:49], 0, v[144:145]
	s_mov_b32 m0, s65
	s_nop 0
	global_load_lds_dwordx4 v[206:207], off
	v_lshl_add_u64 v[206:207], s[48:49], 0, v[148:149]
	s_mov_b32 m0, s66
	s_nop 0
	global_load_lds_dwordx4 v[206:207], off
	s_waitcnt vmcnt(8)
	s_waitcnt lgkmcnt(0)
	s_setprio 1
	s_barrier
	v_mfma_f32_16x16x32_bf16 v[60:63], v[108:111], v[174:177], v[60:63]
	v_mfma_f32_16x16x32_bf16 v[56:59], v[120:123], v[174:177], v[56:59]
	v_mfma_f32_16x16x32_bf16 v[44:47], v[108:111], v[182:185], v[44:47]
	v_mfma_f32_16x16x32_bf16 v[40:43], v[120:123], v[182:185], v[40:43]
	v_mfma_f32_16x16x32_bf16 v[28:31], v[108:111], v[190:193], v[28:31]
	v_mfma_f32_16x16x32_bf16 v[24:27], v[120:123], v[190:193], v[24:27]
	v_mfma_f32_16x16x32_bf16 v[12:15], v[108:111], v[198:201], v[12:15]
	v_mfma_f32_16x16x32_bf16 v[8:11], v[120:123], v[198:201], v[8:11]
	v_mfma_f32_16x16x32_bf16 v[60:63], v[112:115], v[178:181], v[60:63]
	v_mfma_f32_16x16x32_bf16 v[56:59], v[124:127], v[178:181], v[56:59]
	v_mfma_f32_16x16x32_bf16 v[44:47], v[112:115], v[186:189], v[44:47]
	v_mfma_f32_16x16x32_bf16 v[40:43], v[124:127], v[186:189], v[40:43]
	v_mfma_f32_16x16x32_bf16 v[28:31], v[112:115], v[194:197], v[28:31]
	v_mfma_f32_16x16x32_bf16 v[24:27], v[124:127], v[194:197], v[24:27]
	v_mfma_f32_16x16x32_bf16 v[12:15], v[112:115], v[202:205], v[12:15]
	v_mfma_f32_16x16x32_bf16 v[8:11], v[124:127], v[202:205], v[8:11]
	v_mfma_f32_16x16x32_bf16 v[52:55], v[158:161], v[174:177], v[52:55]
	v_mfma_f32_16x16x32_bf16 v[48:51], v[166:169], v[174:177], v[48:51]
	v_mfma_f32_16x16x32_bf16 v[36:39], v[158:161], v[182:185], v[36:39]
	v_mfma_f32_16x16x32_bf16 v[32:35], v[166:169], v[182:185], v[32:35]
	v_mfma_f32_16x16x32_bf16 v[20:23], v[158:161], v[190:193], v[20:23]
	v_mfma_f32_16x16x32_bf16 v[16:19], v[166:169], v[190:193], v[16:19]
	v_mfma_f32_16x16x32_bf16 v[4:7], v[158:161], v[198:201], v[4:7]
	v_mfma_f32_16x16x32_bf16 v[0:3], v[166:169], v[198:201], v[0:3]
	v_mfma_f32_16x16x32_bf16 v[52:55], v[162:165], v[178:181], v[52:55]
	v_mfma_f32_16x16x32_bf16 v[48:51], v[170:173], v[178:181], v[48:51]
	v_mfma_f32_16x16x32_bf16 v[36:39], v[162:165], v[186:189], v[36:39]
	v_mfma_f32_16x16x32_bf16 v[32:35], v[170:173], v[186:189], v[32:35]
	v_mfma_f32_16x16x32_bf16 v[20:23], v[162:165], v[194:197], v[20:23]
	v_mfma_f32_16x16x32_bf16 v[16:19], v[170:173], v[194:197], v[16:19]
	v_mfma_f32_16x16x32_bf16 v[4:7], v[162:165], v[202:205], v[4:7]
	v_mfma_f32_16x16x32_bf16 v[0:3], v[170:173], v[202:205], v[0:3]
	s_barrier
	s_setprio 0
	s_add_i32 s78, s78, 2
	s_add_u32 s76, s76, 0x10000
	s_addc_u32 s77, s77, 0
	s_cmp_gt_u32 s78, 29
	s_mov_b64 s[0:1], s[46:47]
.LBB0_1173:
	v_add_u32_e32 v124, s28, v156
	v_add_u32_e32 v170, s45, v156
	ds_read_b128 v[108:111], v124
	ds_read_b128 v[112:115], v124 offset:1024
	ds_read_b128 v[120:123], v124 offset:2048
	ds_read_b128 v[124:127], v124 offset:3072
	ds_read_b128 v[158:161], v170
	ds_read_b128 v[162:165], v170 offset:1024
	ds_read_b128 v[166:169], v170 offset:2048
	ds_read_b128 v[170:173], v170 offset:3072
	s_add_u32 s46, s0, 0x10000
	s_addc_u32 s47, s1, 0
	s_cmp_eq_u32 s78, 28
	s_cselect_b32 s52, s5, s46
	s_cselect_b32 s53, s4, s47
	s_cselect_b32 s50, s39, s76
	s_cselect_b32 s51, s35, s77
	s_add_u32 s48, s52, 0x8000
	s_addc_u32 s49, s53, 0
	v_lshl_add_u64 v[206:207], s[0:1], 0, v[152:153]
	s_add_i32 m0, s56, 0xc000
	ds_read_b128 v[174:177], v157
	ds_read_b128 v[178:181], v157 offset:1024
	ds_read_b128 v[182:185], v157 offset:2048
	ds_read_b128 v[186:189], v157 offset:3072
	ds_read_b128 v[190:193], v157 offset:4096
	ds_read_b128 v[194:197], v157 offset:5120
	ds_read_b128 v[198:201], v157 offset:6144
	ds_read_b128 v[202:205], v157 offset:7168
	global_load_lds_dwordx4 v[206:207], off
	v_lshl_add_u64 v[206:207], s[0:1], 0, v[154:155]
	s_add_i32 m0, s56, 0xe000
	s_nop 0
	global_load_lds_dwordx4 v[206:207], off
	s_waitcnt vmcnt(8)
	s_waitcnt lgkmcnt(0)
	s_setprio 1
	s_barrier
	v_mfma_f32_16x16x32_bf16 v[140:143], v[108:111], v[174:177], v[140:143]
	v_mfma_f32_16x16x32_bf16 v[136:139], v[120:123], v[174:177], v[136:139]
	v_mfma_f32_16x16x32_bf16 v[116:119], v[108:111], v[182:185], v[116:119]
	v_mfma_f32_16x16x32_bf16 v[104:107], v[120:123], v[182:185], v[104:107]
	v_mfma_f32_16x16x32_bf16 v[92:95], v[108:111], v[190:193], v[92:95]
	v_mfma_f32_16x16x32_bf16 v[88:91], v[120:123], v[190:193], v[88:91]
	v_mfma_f32_16x16x32_bf16 v[76:79], v[108:111], v[198:201], v[76:79]
	v_mfma_f32_16x16x32_bf16 v[72:75], v[120:123], v[198:201], v[72:75]
	v_mfma_f32_16x16x32_bf16 v[140:143], v[112:115], v[178:181], v[140:143]
	v_mfma_f32_16x16x32_bf16 v[136:139], v[124:127], v[178:181], v[136:139]
	v_mfma_f32_16x16x32_bf16 v[116:119], v[112:115], v[186:189], v[116:119]
	v_mfma_f32_16x16x32_bf16 v[104:107], v[124:127], v[186:189], v[104:107]
	v_mfma_f32_16x16x32_bf16 v[92:95], v[112:115], v[194:197], v[92:95]
	v_mfma_f32_16x16x32_bf16 v[88:91], v[124:127], v[194:197], v[88:91]
	v_mfma_f32_16x16x32_bf16 v[76:79], v[112:115], v[202:205], v[76:79]
	v_mfma_f32_16x16x32_bf16 v[72:75], v[124:127], v[202:205], v[72:75]
	v_mfma_f32_16x16x32_bf16 v[132:135], v[158:161], v[174:177], v[132:135]
	v_mfma_f32_16x16x32_bf16 v[128:131], v[166:169], v[174:177], v[128:131]
	v_mfma_f32_16x16x32_bf16 v[100:103], v[158:161], v[182:185], v[100:103]
	v_mfma_f32_16x16x32_bf16 v[96:99], v[166:169], v[182:185], v[96:99]
	v_mfma_f32_16x16x32_bf16 v[84:87], v[158:161], v[190:193], v[84:87]
	v_mfma_f32_16x16x32_bf16 v[80:83], v[166:169], v[190:193], v[80:83]
	v_mfma_f32_16x16x32_bf16 v[68:71], v[158:161], v[198:201], v[68:71]
	v_mfma_f32_16x16x32_bf16 v[64:67], v[166:169], v[198:201], v[64:67]
	v_mfma_f32_16x16x32_bf16 v[132:135], v[162:165], v[178:181], v[132:135]
	v_mfma_f32_16x16x32_bf16 v[128:131], v[170:173], v[178:181], v[128:131]
	v_mfma_f32_16x16x32_bf16 v[100:103], v[162:165], v[186:189], v[100:103]
	v_mfma_f32_16x16x32_bf16 v[96:99], v[170:173], v[186:189], v[96:99]
	v_mfma_f32_16x16x32_bf16 v[84:87], v[162:165], v[194:197], v[84:87]
	v_mfma_f32_16x16x32_bf16 v[80:83], v[170:173], v[194:197], v[80:83]
	v_mfma_f32_16x16x32_bf16 v[68:71], v[162:165], v[202:205], v[68:71]
	v_mfma_f32_16x16x32_bf16 v[64:67], v[170:173], v[202:205], v[64:67]
	s_barrier
	s_setprio 0
	s_mov_b32 m0, s30
	v_lshl_add_u64 v[206:207], s[50:51], 0, v[146:147]
	s_add_u32 s0, s50, 0x4000
	ds_read_b128 v[174:177], v157 offset:16384
	ds_read_b128 v[178:181], v157 offset:17408
	ds_read_b128 v[182:185], v157 offset:18432
	ds_read_b128 v[186:189], v157 offset:19456
	ds_read_b128 v[190:193], v157 offset:20480
	ds_read_b128 v[194:197], v157 offset:21504
	ds_read_b128 v[198:201], v157 offset:22528
	ds_read_b128 v[202:205], v157 offset:23552
	global_load_lds_dwordx4 v[206:207], off
	v_lshl_add_u64 v[206:207], s[50:51], 0, v[150:151]
	s_mov_b32 m0, s31
	s_addc_u32 s1, s51, 0
	global_load_lds_dwordx4 v[206:207], off
	v_lshl_add_u64 v[206:207], s[0:1], 0, v[146:147]
	s_mov_b32 m0, s54
	s_nop 0
	global_load_lds_dwordx4 v[206:207], off
	v_lshl_add_u64 v[206:207], s[0:1], 0, v[150:151]
	s_mov_b32 m0, s55
	s_nop 0
	global_load_lds_dwordx4 v[206:207], off
	v_lshl_add_u64 v[206:207], s[52:53], 0, v[144:145]
	s_mov_b32 m0, s56
	s_nop 0
	global_load_lds_dwordx4 v[206:207], off
	v_lshl_add_u64 v[206:207], s[52:53], 0, v[148:149]
	s_mov_b32 m0, s57
	s_nop 0
	global_load_lds_dwordx4 v[206:207], off
	s_waitcnt vmcnt(8)
	s_waitcnt lgkmcnt(0)
	s_setprio 1
	s_barrier
	v_mfma_f32_16x16x32_bf16 v[60:63], v[108:111], v[174:177], v[60:63]
	v_mfma_f32_16x16x32_bf16 v[56:59], v[120:123], v[174:177], v[56:59]
	v_mfma_f32_16x16x32_bf16 v[44:47], v[108:111], v[182:185], v[44:47]
	v_mfma_f32_16x16x32_bf16 v[40:43], v[120:123], v[182:185], v[40:43]
	v_mfma_f32_16x16x32_bf16 v[28:31], v[108:111], v[190:193], v[28:31]
	v_mfma_f32_16x16x32_bf16 v[24:27], v[120:123], v[190:193], v[24:27]
	v_mfma_f32_16x16x32_bf16 v[12:15], v[108:111], v[198:201], v[12:15]
	v_mfma_f32_16x16x32_bf16 v[8:11], v[120:123], v[198:201], v[8:11]
	v_mfma_f32_16x16x32_bf16 v[60:63], v[112:115], v[178:181], v[60:63]
	v_mfma_f32_16x16x32_bf16 v[56:59], v[124:127], v[178:181], v[56:59]
	v_mfma_f32_16x16x32_bf16 v[44:47], v[112:115], v[186:189], v[44:47]
	v_mfma_f32_16x16x32_bf16 v[40:43], v[124:127], v[186:189], v[40:43]
	v_mfma_f32_16x16x32_bf16 v[28:31], v[112:115], v[194:197], v[28:31]
	v_mfma_f32_16x16x32_bf16 v[24:27], v[124:127], v[194:197], v[24:27]
	v_mfma_f32_16x16x32_bf16 v[12:15], v[112:115], v[202:205], v[12:15]
	v_mfma_f32_16x16x32_bf16 v[8:11], v[124:127], v[202:205], v[8:11]
	v_mfma_f32_16x16x32_bf16 v[52:55], v[158:161], v[174:177], v[52:55]
	v_mfma_f32_16x16x32_bf16 v[48:51], v[166:169], v[174:177], v[48:51]
	v_mfma_f32_16x16x32_bf16 v[36:39], v[158:161], v[182:185], v[36:39]
	v_mfma_f32_16x16x32_bf16 v[32:35], v[166:169], v[182:185], v[32:35]
	v_mfma_f32_16x16x32_bf16 v[20:23], v[158:161], v[190:193], v[20:23]
	v_mfma_f32_16x16x32_bf16 v[16:19], v[166:169], v[190:193], v[16:19]
	v_mfma_f32_16x16x32_bf16 v[4:7], v[158:161], v[198:201], v[4:7]
	v_mfma_f32_16x16x32_bf16 v[0:3], v[166:169], v[198:201], v[0:3]
	v_mfma_f32_16x16x32_bf16 v[52:55], v[162:165], v[178:181], v[52:55]
	v_mfma_f32_16x16x32_bf16 v[48:51], v[170:173], v[178:181], v[48:51]
	v_mfma_f32_16x16x32_bf16 v[36:39], v[162:165], v[186:189], v[36:39]
	v_mfma_f32_16x16x32_bf16 v[32:35], v[170:173], v[186:189], v[32:35]
	v_mfma_f32_16x16x32_bf16 v[20:23], v[162:165], v[194:197], v[20:23]
	v_mfma_f32_16x16x32_bf16 v[16:19], v[170:173], v[194:197], v[16:19]
	v_mfma_f32_16x16x32_bf16 v[4:7], v[162:165], v[202:205], v[4:7]
	v_mfma_f32_16x16x32_bf16 v[0:3], v[170:173], v[202:205], v[0:3]
	s_barrier
	s_setprio 0
	v_add_u32_e32 v124, s62, v156
	v_add_u32_e32 v170, s67, v156
	ds_read_b128 v[108:111], v124
	ds_read_b128 v[112:115], v124 offset:1024
	ds_read_b128 v[120:123], v124 offset:2048
	ds_read_b128 v[124:127], v124 offset:3072
	ds_read_b128 v[158:161], v170
	ds_read_b128 v[162:165], v170 offset:1024
	ds_read_b128 v[166:169], v170 offset:2048
	ds_read_b128 v[170:173], v170 offset:3072
	s_add_u32 s0, s52, 0x4000
	s_addc_u32 s1, s53, 0
	s_mov_b32 m0, s58
	v_lshl_add_u64 v[206:207], s[0:1], 0, v[144:145]
	ds_read_b128 v[174:177], v157 offset:32768
	ds_read_b128 v[178:181], v157 offset:33792
	ds_read_b128 v[182:185], v157 offset:34816
	ds_read_b128 v[186:189], v157 offset:35840
	ds_read_b128 v[190:193], v157 offset:36864
	ds_read_b128 v[194:197], v157 offset:37888
	ds_read_b128 v[198:201], v157 offset:38912
	ds_read_b128 v[202:205], v157 offset:39936
	global_load_lds_dwordx4 v[206:207], off
	v_lshl_add_u64 v[206:207], s[0:1], 0, v[148:149]
	s_mov_b32 m0, s59
	s_nop 0
	global_load_lds_dwordx4 v[206:207], off
	s_waitcnt vmcnt(8)
	s_waitcnt lgkmcnt(0)
	s_setprio 1
	s_barrier
	v_mfma_f32_16x16x32_bf16 v[140:143], v[108:111], v[174:177], v[140:143]
	v_mfma_f32_16x16x32_bf16 v[136:139], v[120:123], v[174:177], v[136:139]
	v_mfma_f32_16x16x32_bf16 v[116:119], v[108:111], v[182:185], v[116:119]
	v_mfma_f32_16x16x32_bf16 v[104:107], v[120:123], v[182:185], v[104:107]
	v_mfma_f32_16x16x32_bf16 v[92:95], v[108:111], v[190:193], v[92:95]
	v_mfma_f32_16x16x32_bf16 v[88:91], v[120:123], v[190:193], v[88:91]
	v_mfma_f32_16x16x32_bf16 v[76:79], v[108:111], v[198:201], v[76:79]
	v_mfma_f32_16x16x32_bf16 v[72:75], v[120:123], v[198:201], v[72:75]
	v_mfma_f32_16x16x32_bf16 v[140:143], v[112:115], v[178:181], v[140:143]
	v_mfma_f32_16x16x32_bf16 v[136:139], v[124:127], v[178:181], v[136:139]
	v_mfma_f32_16x16x32_bf16 v[116:119], v[112:115], v[186:189], v[116:119]
	v_mfma_f32_16x16x32_bf16 v[104:107], v[124:127], v[186:189], v[104:107]
	v_mfma_f32_16x16x32_bf16 v[92:95], v[112:115], v[194:197], v[92:95]
	v_mfma_f32_16x16x32_bf16 v[88:91], v[124:127], v[194:197], v[88:91]
	v_mfma_f32_16x16x32_bf16 v[76:79], v[112:115], v[202:205], v[76:79]
	v_mfma_f32_16x16x32_bf16 v[72:75], v[124:127], v[202:205], v[72:75]
	v_mfma_f32_16x16x32_bf16 v[132:135], v[158:161], v[174:177], v[132:135]
	v_mfma_f32_16x16x32_bf16 v[128:131], v[166:169], v[174:177], v[128:131]
	v_mfma_f32_16x16x32_bf16 v[100:103], v[158:161], v[182:185], v[100:103]
	v_mfma_f32_16x16x32_bf16 v[96:99], v[166:169], v[182:185], v[96:99]
	v_mfma_f32_16x16x32_bf16 v[84:87], v[158:161], v[190:193], v[84:87]
	v_mfma_f32_16x16x32_bf16 v[80:83], v[166:169], v[190:193], v[80:83]
	v_mfma_f32_16x16x32_bf16 v[68:71], v[158:161], v[198:201], v[68:71]
	v_mfma_f32_16x16x32_bf16 v[64:67], v[166:169], v[198:201], v[64:67]
	v_mfma_f32_16x16x32_bf16 v[132:135], v[162:165], v[178:181], v[132:135]
	v_mfma_f32_16x16x32_bf16 v[128:131], v[170:173], v[178:181], v[128:131]
	v_mfma_f32_16x16x32_bf16 v[100:103], v[162:165], v[186:189], v[100:103]
	v_mfma_f32_16x16x32_bf16 v[96:99], v[170:173], v[186:189], v[96:99]
	v_mfma_f32_16x16x32_bf16 v[84:87], v[162:165], v[194:197], v[84:87]
	v_mfma_f32_16x16x32_bf16 v[80:83], v[170:173], v[194:197], v[80:83]
	v_mfma_f32_16x16x32_bf16 v[68:71], v[162:165], v[202:205], v[68:71]
	v_mfma_f32_16x16x32_bf16 v[64:67], v[170:173], v[202:205], v[64:67]
	s_barrier
	s_setprio 0
	s_add_u32 s0, s50, 0x8000
	s_addc_u32 s1, s51, 0
	s_mov_b32 m0, s63
	v_lshl_add_u64 v[206:207], s[0:1], 0, v[146:147]
	ds_read_b128 v[174:177], v157 offset:49152
	ds_read_b128 v[178:181], v157 offset:50176
	ds_read_b128 v[182:185], v157 offset:51200
	ds_read_b128 v[186:189], v157 offset:52224
	ds_read_b128 v[190:193], v157 offset:53248
	ds_read_b128 v[194:197], v157 offset:54272
	ds_read_b128 v[198:201], v157 offset:55296
	ds_read_b128 v[202:205], v157 offset:56320
	global_load_lds_dwordx4 v[206:207], off
	v_lshl_add_u64 v[206:207], s[0:1], 0, v[150:151]
	s_add_u32 s0, s50, 0xc000
	s_mov_b32 m0, s64
	s_addc_u32 s1, s51, 0
	global_load_lds_dwordx4 v[206:207], off
	v_lshl_add_u64 v[206:207], s[0:1], 0, v[146:147]
	s_mov_b32 m0, s68
	s_nop 0
	global_load_lds_dwordx4 v[206:207], off
	v_lshl_add_u64 v[206:207], s[0:1], 0, v[150:151]
	s_mov_b32 m0, s69
	s_nop 0
	global_load_lds_dwordx4 v[206:207], off
	v_lshl_add_u64 v[206:207], s[48:49], 0, v[144:145]
	s_mov_b32 m0, s65
	s_nop 0
	global_load_lds_dwordx4 v[206:207], off
	v_lshl_add_u64 v[206:207], s[48:49], 0, v[148:149]
	s_mov_b32 m0, s66
	s_nop 0
	global_load_lds_dwordx4 v[206:207], off
	s_waitcnt vmcnt(8)
	s_waitcnt lgkmcnt(0)
	s_setprio 1
	s_barrier
	v_mfma_f32_16x16x32_bf16 v[60:63], v[108:111], v[174:177], v[60:63]
	v_mfma_f32_16x16x32_bf16 v[56:59], v[120:123], v[174:177], v[56:59]
	v_mfma_f32_16x16x32_bf16 v[44:47], v[108:111], v[182:185], v[44:47]
	v_mfma_f32_16x16x32_bf16 v[40:43], v[120:123], v[182:185], v[40:43]
	v_mfma_f32_16x16x32_bf16 v[28:31], v[108:111], v[190:193], v[28:31]
	v_mfma_f32_16x16x32_bf16 v[24:27], v[120:123], v[190:193], v[24:27]
	v_mfma_f32_16x16x32_bf16 v[12:15], v[108:111], v[198:201], v[12:15]
	v_mfma_f32_16x16x32_bf16 v[8:11], v[120:123], v[198:201], v[8:11]
	v_mfma_f32_16x16x32_bf16 v[60:63], v[112:115], v[178:181], v[60:63]
	v_mfma_f32_16x16x32_bf16 v[56:59], v[124:127], v[178:181], v[56:59]
	v_mfma_f32_16x16x32_bf16 v[44:47], v[112:115], v[186:189], v[44:47]
	v_mfma_f32_16x16x32_bf16 v[40:43], v[124:127], v[186:189], v[40:43]
	v_mfma_f32_16x16x32_bf16 v[28:31], v[112:115], v[194:197], v[28:31]
	v_mfma_f32_16x16x32_bf16 v[24:27], v[124:127], v[194:197], v[24:27]
	v_mfma_f32_16x16x32_bf16 v[12:15], v[112:115], v[202:205], v[12:15]
	v_mfma_f32_16x16x32_bf16 v[8:11], v[124:127], v[202:205], v[8:11]
	v_mfma_f32_16x16x32_bf16 v[52:55], v[158:161], v[174:177], v[52:55]
	v_mfma_f32_16x16x32_bf16 v[48:51], v[166:169], v[174:177], v[48:51]
	v_mfma_f32_16x16x32_bf16 v[36:39], v[158:161], v[182:185], v[36:39]
	v_mfma_f32_16x16x32_bf16 v[32:35], v[166:169], v[182:185], v[32:35]
	v_mfma_f32_16x16x32_bf16 v[20:23], v[158:161], v[190:193], v[20:23]
	v_mfma_f32_16x16x32_bf16 v[16:19], v[166:169], v[190:193], v[16:19]
	v_mfma_f32_16x16x32_bf16 v[4:7], v[158:161], v[198:201], v[4:7]
	v_mfma_f32_16x16x32_bf16 v[0:3], v[166:169], v[198:201], v[0:3]
	v_mfma_f32_16x16x32_bf16 v[52:55], v[162:165], v[178:181], v[52:55]
	v_mfma_f32_16x16x32_bf16 v[48:51], v[170:173], v[178:181], v[48:51]
	v_mfma_f32_16x16x32_bf16 v[36:39], v[162:165], v[186:189], v[36:39]
	v_mfma_f32_16x16x32_bf16 v[32:35], v[170:173], v[186:189], v[32:35]
	v_mfma_f32_16x16x32_bf16 v[20:23], v[162:165], v[194:197], v[20:23]
	v_mfma_f32_16x16x32_bf16 v[16:19], v[170:173], v[194:197], v[16:19]
	v_mfma_f32_16x16x32_bf16 v[4:7], v[162:165], v[202:205], v[4:7]
	v_mfma_f32_16x16x32_bf16 v[0:3], v[170:173], v[202:205], v[0:3]
	s_barrier
	s_setprio 0
	s_add_i32 s78, s78, 2
	s_add_u32 s76, s76, 0x10000
	s_addc_u32 s77, s77, 0
	s_cmp_gt_u32 s78, 29
	s_mov_b64 s[0:1], s[46:47]
	s_cbranch_scc0 .LBB0_1173
	s_and_b64 vcc, exec, s[24:25]
	s_cbranch_vccz .LBB0_1176
	s_barrier

.LBB0_1247:
	s_ashr_i32 s35, s34, 31
	s_lshl_b64 s[4:5], s[34:35], 22
	s_add_u32 s38, s17, s4
	s_addc_u32 s39, s18, s5
	s_and_b64 s[4:5], s[36:37], exec
	s_cselect_b32 s4, s39, s1
	s_cselect_b32 s5, s38, s0
	s_ashr_i32 s25, s24, 31
	s_lshl_b64 s[40:41], s[24:25], 22
	s_add_u32 s40, s19, s40
	s_addc_u32 s41, s28, s41
	s_and_b64 s[46:47], s[36:37], exec
	s_cselect_b32 s25, s41, s45
	s_cselect_b32 s35, s40, s44
	s_add_u32 s74, s44, 0x10000
	s_addc_u32 s75, s45, 0
	s_mov_b32 s76, -2
	v_add_u32_e32 v92, s30, v206
	v_add_u32_e32 v156, s52, v206
	ds_read_b128 v[72:75], v92
	ds_read_b128 v[76:79], v92 offset:1024
	ds_read_b128 v[84:87], v92 offset:2048
	ds_read_b128 v[92:95], v92 offset:3072
	ds_read_b128 v[144:147], v156
	ds_read_b128 v[148:151], v156 offset:1024
	ds_read_b128 v[152:155], v156 offset:2048
	ds_read_b128 v[156:159], v156 offset:3072
	s_add_u32 s44, s0, 0x10000
	s_addc_u32 s45, s1, 0
	s_cmpk_eq_i32 s76, 0x7c
	s_cselect_b32 s50, s5, s44
	s_cselect_b32 s51, s4, s45
	s_cselect_b32 s48, s35, s74
	s_cselect_b32 s49, s25, s75
	s_add_u32 s46, s50, 0x8000
	s_addc_u32 s47, s51, 0
	v_lshl_add_u64 v[204:205], s[0:1], 0, v[180:181]
	s_add_i32 m0, s56, 0xc000
	ds_read_b128 v[160:163], v207
	ds_read_b128 v[164:167], v207 offset:1024
	ds_read_b128 v[168:171], v207 offset:2048
	ds_read_b128 v[184:187], v207 offset:3072
	ds_read_b128 v[188:191], v207 offset:4096
	ds_read_b128 v[192:195], v207 offset:5120
	ds_read_b128 v[196:199], v207 offset:6144
	ds_read_b128 v[200:203], v207 offset:7168
	global_load_lds_dwordx4 v[204:205], off
	v_lshl_add_u64 v[204:205], s[0:1], 0, v[182:183]
	s_add_i32 m0, s56, 0xe000
	s_nop 0
	global_load_lds_dwordx4 v[204:205], off
	s_waitcnt vmcnt(8)
	s_waitcnt lgkmcnt(0)
	s_setprio 1
	s_barrier
	v_mfma_f32_16x16x32_bf16 v[140:143], v[72:75], v[160:163], 0
	v_mfma_f32_16x16x32_bf16 v[136:139], v[84:87], v[160:163], 0
	v_mfma_f32_16x16x32_bf16 v[124:127], v[72:75], v[168:171], 0
	v_mfma_f32_16x16x32_bf16 v[120:123], v[84:87], v[168:171], 0
	v_mfma_f32_16x16x32_bf16 v[108:111], v[72:75], v[188:191], 0
	v_mfma_f32_16x16x32_bf16 v[104:107], v[84:87], v[188:191], 0
	v_mfma_f32_16x16x32_bf16 v[88:91], v[72:75], v[196:199], 0
	v_mfma_f32_16x16x32_bf16 v[80:83], v[84:87], v[196:199], 0
	v_mfma_f32_16x16x32_bf16 v[140:143], v[76:79], v[164:167], v[140:143]
	v_mfma_f32_16x16x32_bf16 v[136:139], v[92:95], v[164:167], v[136:139]
	v_mfma_f32_16x16x32_bf16 v[124:127], v[76:79], v[184:187], v[124:127]
	v_mfma_f32_16x16x32_bf16 v[120:123], v[92:95], v[184:187], v[120:123]
	v_mfma_f32_16x16x32_bf16 v[108:111], v[76:79], v[192:195], v[108:111]
	v_mfma_f32_16x16x32_bf16 v[104:107], v[92:95], v[192:195], v[104:107]
	v_mfma_f32_16x16x32_bf16 v[88:91], v[76:79], v[200:203], v[88:91]
	v_mfma_f32_16x16x32_bf16 v[80:83], v[92:95], v[200:203], v[80:83]
	v_mfma_f32_16x16x32_bf16 v[132:135], v[144:147], v[160:163], 0
	v_mfma_f32_16x16x32_bf16 v[128:131], v[152:155], v[160:163], 0
	v_mfma_f32_16x16x32_bf16 v[116:119], v[144:147], v[168:171], 0
	v_mfma_f32_16x16x32_bf16 v[112:115], v[152:155], v[168:171], 0
	v_mfma_f32_16x16x32_bf16 v[100:103], v[144:147], v[188:191], 0
	v_mfma_f32_16x16x32_bf16 v[96:99], v[152:155], v[188:191], 0
	v_mfma_f32_16x16x32_bf16 v[68:71], v[144:147], v[196:199], 0
	v_mfma_f32_16x16x32_bf16 v[64:67], v[152:155], v[196:199], 0
	v_mfma_f32_16x16x32_bf16 v[132:135], v[148:151], v[164:167], v[132:135]
	v_mfma_f32_16x16x32_bf16 v[128:131], v[156:159], v[164:167], v[128:131]
	v_mfma_f32_16x16x32_bf16 v[116:119], v[148:151], v[184:187], v[116:119]
	v_mfma_f32_16x16x32_bf16 v[112:115], v[156:159], v[184:187], v[112:115]
	v_mfma_f32_16x16x32_bf16 v[100:103], v[148:151], v[192:195], v[100:103]
	v_mfma_f32_16x16x32_bf16 v[96:99], v[156:159], v[192:195], v[96:99]
	v_mfma_f32_16x16x32_bf16 v[68:71], v[148:151], v[200:203], v[68:71]
	v_mfma_f32_16x16x32_bf16 v[64:67], v[156:159], v[200:203], v[64:67]
	s_barrier
	s_setprio 0
	s_mov_b32 m0, s31
	v_lshl_add_u64 v[204:205], s[48:49], 0, v[174:175]
	s_add_u32 s0, s48, 0x4000
	ds_read_b128 v[160:163], v207 offset:16384
	ds_read_b128 v[164:167], v207 offset:17408
	ds_read_b128 v[168:171], v207 offset:18432
	ds_read_b128 v[184:187], v207 offset:19456
	ds_read_b128 v[188:191], v207 offset:20480
	ds_read_b128 v[192:195], v207 offset:21504
	ds_read_b128 v[196:199], v207 offset:22528
	ds_read_b128 v[200:203], v207 offset:23552
	global_load_lds_dwordx4 v[204:205], off
	v_lshl_add_u64 v[204:205], s[48:49], 0, v[178:179]
	s_mov_b32 m0, s43
	s_addc_u32 s1, s49, 0
	global_load_lds_dwordx4 v[204:205], off
	v_lshl_add_u64 v[204:205], s[0:1], 0, v[174:175]
	s_mov_b32 m0, s53
	s_nop 0
	global_load_lds_dwordx4 v[204:205], off
	v_lshl_add_u64 v[204:205], s[0:1], 0, v[178:179]
	s_mov_b32 m0, s54
	s_nop 0
	global_load_lds_dwordx4 v[204:205], off
	v_lshl_add_u64 v[204:205], s[50:51], 0, v[172:173]
	s_mov_b32 m0, s56
	s_nop 0
	global_load_lds_dwordx4 v[204:205], off
	v_lshl_add_u64 v[204:205], s[50:51], 0, v[176:177]
	s_mov_b32 m0, s57
	s_nop 0
	global_load_lds_dwordx4 v[204:205], off
	s_waitcnt vmcnt(8)
	s_waitcnt lgkmcnt(0)
	s_setprio 1
	s_barrier
	v_mfma_f32_16x16x32_bf16 v[60:63], v[72:75], v[160:163], 0
	v_mfma_f32_16x16x32_bf16 v[56:59], v[84:87], v[160:163], 0
	v_mfma_f32_16x16x32_bf16 v[44:47], v[72:75], v[168:171], 0
	v_mfma_f32_16x16x32_bf16 v[40:43], v[84:87], v[168:171], 0
	v_mfma_f32_16x16x32_bf16 v[28:31], v[72:75], v[188:191], 0
	v_mfma_f32_16x16x32_bf16 v[24:27], v[84:87], v[188:191], 0
	v_mfma_f32_16x16x32_bf16 v[12:15], v[72:75], v[196:199], 0
	v_mfma_f32_16x16x32_bf16 v[8:11], v[84:87], v[196:199], 0
	v_mfma_f32_16x16x32_bf16 v[60:63], v[76:79], v[164:167], v[60:63]
	v_mfma_f32_16x16x32_bf16 v[56:59], v[92:95], v[164:167], v[56:59]
	v_mfma_f32_16x16x32_bf16 v[44:47], v[76:79], v[184:187], v[44:47]
	v_mfma_f32_16x16x32_bf16 v[40:43], v[92:95], v[184:187], v[40:43]
	v_mfma_f32_16x16x32_bf16 v[28:31], v[76:79], v[192:195], v[28:31]
	v_mfma_f32_16x16x32_bf16 v[24:27], v[92:95], v[192:195], v[24:27]
	v_mfma_f32_16x16x32_bf16 v[12:15], v[76:79], v[200:203], v[12:15]
	v_mfma_f32_16x16x32_bf16 v[8:11], v[92:95], v[200:203], v[8:11]
	v_mfma_f32_16x16x32_bf16 v[52:55], v[144:147], v[160:163], 0
	v_mfma_f32_16x16x32_bf16 v[48:51], v[152:155], v[160:163], 0
	v_mfma_f32_16x16x32_bf16 v[36:39], v[144:147], v[168:171], 0
	v_mfma_f32_16x16x32_bf16 v[32:35], v[152:155], v[168:171], 0
	v_mfma_f32_16x16x32_bf16 v[20:23], v[144:147], v[188:191], 0
	v_mfma_f32_16x16x32_bf16 v[16:19], v[152:155], v[188:191], 0
	v_mfma_f32_16x16x32_bf16 v[4:7], v[144:147], v[196:199], 0
	v_mfma_f32_16x16x32_bf16 v[0:3], v[152:155], v[196:199], 0
	v_mfma_f32_16x16x32_bf16 v[52:55], v[148:151], v[164:167], v[52:55]
	v_mfma_f32_16x16x32_bf16 v[48:51], v[156:159], v[164:167], v[48:51]
	v_mfma_f32_16x16x32_bf16 v[36:39], v[148:151], v[184:187], v[36:39]
	v_mfma_f32_16x16x32_bf16 v[32:35], v[156:159], v[184:187], v[32:35]
	v_mfma_f32_16x16x32_bf16 v[20:23], v[148:151], v[192:195], v[20:23]
	v_mfma_f32_16x16x32_bf16 v[16:19], v[156:159], v[192:195], v[16:19]
	v_mfma_f32_16x16x32_bf16 v[4:7], v[148:151], v[200:203], v[4:7]
	v_mfma_f32_16x16x32_bf16 v[0:3], v[156:159], v[200:203], v[0:3]
	s_barrier
	s_setprio 0
	v_add_u32_e32 v92, s64, v206
	v_add_u32_e32 v156, s69, v206
	ds_read_b128 v[72:75], v92
	ds_read_b128 v[76:79], v92 offset:1024
	ds_read_b128 v[84:87], v92 offset:2048
	ds_read_b128 v[92:95], v92 offset:3072
	ds_read_b128 v[144:147], v156
	ds_read_b128 v[148:151], v156 offset:1024
	ds_read_b128 v[152:155], v156 offset:2048
	ds_read_b128 v[156:159], v156 offset:3072
	s_add_u32 s0, s50, 0x4000
	s_addc_u32 s1, s51, 0
	s_mov_b32 m0, s58
	v_lshl_add_u64 v[204:205], s[0:1], 0, v[172:173]
	ds_read_b128 v[160:163], v207 offset:32768
	ds_read_b128 v[164:167], v207 offset:33792
	ds_read_b128 v[168:171], v207 offset:34816
	ds_read_b128 v[184:187], v207 offset:35840
	ds_read_b128 v[188:191], v207 offset:36864
	ds_read_b128 v[192:195], v207 offset:37888
	ds_read_b128 v[196:199], v207 offset:38912
	ds_read_b128 v[200:203], v207 offset:39936
	global_load_lds_dwordx4 v[204:205], off
	v_lshl_add_u64 v[204:205], s[0:1], 0, v[176:177]
	s_mov_b32 m0, s59
	s_nop 0
	global_load_lds_dwordx4 v[204:205], off
	s_waitcnt vmcnt(8)
	s_waitcnt lgkmcnt(0)
	s_setprio 1
	s_barrier
	v_mfma_f32_16x16x32_bf16 v[140:143], v[72:75], v[160:163], v[140:143]
	v_mfma_f32_16x16x32_bf16 v[136:139], v[84:87], v[160:163], v[136:139]
	v_mfma_f32_16x16x32_bf16 v[124:127], v[72:75], v[168:171], v[124:127]
	v_mfma_f32_16x16x32_bf16 v[120:123], v[84:87], v[168:171], v[120:123]
	v_mfma_f32_16x16x32_bf16 v[108:111], v[72:75], v[188:191], v[108:111]
	v_mfma_f32_16x16x32_bf16 v[104:107], v[84:87], v[188:191], v[104:107]
	v_mfma_f32_16x16x32_bf16 v[88:91], v[72:75], v[196:199], v[88:91]
	v_mfma_f32_16x16x32_bf16 v[80:83], v[84:87], v[196:199], v[80:83]
	v_mfma_f32_16x16x32_bf16 v[140:143], v[76:79], v[164:167], v[140:143]
	v_mfma_f32_16x16x32_bf16 v[136:139], v[92:95], v[164:167], v[136:139]
	v_mfma_f32_16x16x32_bf16 v[124:127], v[76:79], v[184:187], v[124:127]
	v_mfma_f32_16x16x32_bf16 v[120:123], v[92:95], v[184:187], v[120:123]
	v_mfma_f32_16x16x32_bf16 v[108:111], v[76:79], v[192:195], v[108:111]
	v_mfma_f32_16x16x32_bf16 v[104:107], v[92:95], v[192:195], v[104:107]
	v_mfma_f32_16x16x32_bf16 v[88:91], v[76:79], v[200:203], v[88:91]
	v_mfma_f32_16x16x32_bf16 v[80:83], v[92:95], v[200:203], v[80:83]
	v_mfma_f32_16x16x32_bf16 v[132:135], v[144:147], v[160:163], v[132:135]
	v_mfma_f32_16x16x32_bf16 v[128:131], v[152:155], v[160:163], v[128:131]
	v_mfma_f32_16x16x32_bf16 v[116:119], v[144:147], v[168:171], v[116:119]
	v_mfma_f32_16x16x32_bf16 v[112:115], v[152:155], v[168:171], v[112:115]
	v_mfma_f32_16x16x32_bf16 v[100:103], v[144:147], v[188:191], v[100:103]
	v_mfma_f32_16x16x32_bf16 v[96:99], v[152:155], v[188:191], v[96:99]
	v_mfma_f32_16x16x32_bf16 v[68:71], v[144:147], v[196:199], v[68:71]
	v_mfma_f32_16x16x32_bf16 v[64:67], v[152:155], v[196:199], v[64:67]
	v_mfma_f32_16x16x32_bf16 v[132:135], v[148:151], v[164:167], v[132:135]
	v_mfma_f32_16x16x32_bf16 v[128:131], v[156:159], v[164:167], v[128:131]
	v_mfma_f32_16x16x32_bf16 v[116:119], v[148:151], v[184:187], v[116:119]
	v_mfma_f32_16x16x32_bf16 v[112:115], v[156:159], v[184:187], v[112:115]
	v_mfma_f32_16x16x32_bf16 v[100:103], v[148:151], v[192:195], v[100:103]
	v_mfma_f32_16x16x32_bf16 v[96:99], v[156:159], v[192:195], v[96:99]
	v_mfma_f32_16x16x32_bf16 v[68:71], v[148:151], v[200:203], v[68:71]
	v_mfma_f32_16x16x32_bf16 v[64:67], v[156:159], v[200:203], v[64:67]
	s_barrier
	s_setprio 0
	s_add_u32 s0, s48, 0x8000
	s_addc_u32 s1, s49, 0
	s_mov_b32 m0, s65
	v_lshl_add_u64 v[204:205], s[0:1], 0, v[174:175]
	ds_read_b128 v[160:163], v207 offset:49152
	ds_read_b128 v[164:167], v207 offset:50176
	ds_read_b128 v[168:171], v207 offset:51200
	ds_read_b128 v[184:187], v207 offset:52224
	ds_read_b128 v[188:191], v207 offset:53248
	ds_read_b128 v[192:195], v207 offset:54272
	ds_read_b128 v[196:199], v207 offset:55296
	ds_read_b128 v[200:203], v207 offset:56320
	global_load_lds_dwordx4 v[204:205], off
	v_lshl_add_u64 v[204:205], s[0:1], 0, v[178:179]
	s_add_u32 s0, s48, 0xc000
	s_mov_b32 m0, s66
	s_addc_u32 s1, s49, 0
	global_load_lds_dwordx4 v[204:205], off
	v_lshl_add_u64 v[204:205], s[0:1], 0, v[174:175]
	s_mov_b32 m0, s70
	s_nop 0
	global_load_lds_dwordx4 v[204:205], off
	v_lshl_add_u64 v[204:205], s[0:1], 0, v[178:179]
	s_mov_b32 m0, s71
	s_nop 0
	global_load_lds_dwordx4 v[204:205], off
	v_lshl_add_u64 v[204:205], s[46:47], 0, v[172:173]
	s_mov_b32 m0, s67
	s_nop 0
	global_load_lds_dwordx4 v[204:205], off
	v_lshl_add_u64 v[204:205], s[46:47], 0, v[176:177]
	s_mov_b32 m0, s68
	s_nop 0
	global_load_lds_dwordx4 v[204:205], off
	s_waitcnt vmcnt(8)
	s_waitcnt lgkmcnt(0)
	s_setprio 1
	s_barrier
	v_mfma_f32_16x16x32_bf16 v[60:63], v[72:75], v[160:163], v[60:63]
	v_mfma_f32_16x16x32_bf16 v[56:59], v[84:87], v[160:163], v[56:59]
	v_mfma_f32_16x16x32_bf16 v[44:47], v[72:75], v[168:171], v[44:47]
	v_mfma_f32_16x16x32_bf16 v[40:43], v[84:87], v[168:171], v[40:43]
	v_mfma_f32_16x16x32_bf16 v[28:31], v[72:75], v[188:191], v[28:31]
	v_mfma_f32_16x16x32_bf16 v[24:27], v[84:87], v[188:191], v[24:27]
	v_mfma_f32_16x16x32_bf16 v[12:15], v[72:75], v[196:199], v[12:15]
	v_mfma_f32_16x16x32_bf16 v[8:11], v[84:87], v[196:199], v[8:11]
	v_mfma_f32_16x16x32_bf16 v[60:63], v[76:79], v[164:167], v[60:63]
	v_mfma_f32_16x16x32_bf16 v[56:59], v[92:95], v[164:167], v[56:59]
	v_mfma_f32_16x16x32_bf16 v[44:47], v[76:79], v[184:187], v[44:47]
	v_mfma_f32_16x16x32_bf16 v[40:43], v[92:95], v[184:187], v[40:43]
	v_mfma_f32_16x16x32_bf16 v[28:31], v[76:79], v[192:195], v[28:31]
	v_mfma_f32_16x16x32_bf16 v[24:27], v[92:95], v[192:195], v[24:27]
	v_mfma_f32_16x16x32_bf16 v[12:15], v[76:79], v[200:203], v[12:15]
	v_mfma_f32_16x16x32_bf16 v[8:11], v[92:95], v[200:203], v[8:11]
	v_mfma_f32_16x16x32_bf16 v[52:55], v[144:147], v[160:163], v[52:55]
	v_mfma_f32_16x16x32_bf16 v[48:51], v[152:155], v[160:163], v[48:51]
	v_mfma_f32_16x16x32_bf16 v[36:39], v[144:147], v[168:171], v[36:39]
	v_mfma_f32_16x16x32_bf16 v[32:35], v[152:155], v[168:171], v[32:35]
	v_mfma_f32_16x16x32_bf16 v[20:23], v[144:147], v[188:191], v[20:23]
	v_mfma_f32_16x16x32_bf16 v[16:19], v[152:155], v[188:191], v[16:19]
	v_mfma_f32_16x16x32_bf16 v[4:7], v[144:147], v[196:199], v[4:7]
	v_mfma_f32_16x16x32_bf16 v[0:3], v[152:155], v[196:199], v[0:3]
	v_mfma_f32_16x16x32_bf16 v[52:55], v[148:151], v[164:167], v[52:55]
	v_mfma_f32_16x16x32_bf16 v[48:51], v[156:159], v[164:167], v[48:51]
	v_mfma_f32_16x16x32_bf16 v[36:39], v[148:151], v[184:187], v[36:39]
	v_mfma_f32_16x16x32_bf16 v[32:35], v[156:159], v[184:187], v[32:35]
	v_mfma_f32_16x16x32_bf16 v[20:23], v[148:151], v[192:195], v[20:23]
	v_mfma_f32_16x16x32_bf16 v[16:19], v[156:159], v[192:195], v[16:19]
	v_mfma_f32_16x16x32_bf16 v[4:7], v[148:151], v[200:203], v[4:7]
	v_mfma_f32_16x16x32_bf16 v[0:3], v[156:159], v[200:203], v[0:3]
	s_barrier
	s_setprio 0
	s_add_i32 s76, s76, 2
	s_add_u32 s74, s74, 0x10000
	s_addc_u32 s75, s75, 0
	s_cmpk_gt_u32 s76, 0x7d
	s_mov_b64 s[0:1], s[44:45]
.LBB0_1248:
	v_add_u32_e32 v92, s30, v206
	v_add_u32_e32 v156, s52, v206
	ds_read_b128 v[72:75], v92
	ds_read_b128 v[76:79], v92 offset:1024
	ds_read_b128 v[84:87], v92 offset:2048
	ds_read_b128 v[92:95], v92 offset:3072
	ds_read_b128 v[144:147], v156
	ds_read_b128 v[148:151], v156 offset:1024
	ds_read_b128 v[152:155], v156 offset:2048
	ds_read_b128 v[156:159], v156 offset:3072
	s_add_u32 s44, s0, 0x10000
	s_addc_u32 s45, s1, 0
	s_cmpk_eq_i32 s76, 0x7c
	s_cselect_b32 s50, s5, s44
	s_cselect_b32 s51, s4, s45
	s_cselect_b32 s48, s35, s74
	s_cselect_b32 s49, s25, s75
	s_add_u32 s46, s50, 0x8000
	s_addc_u32 s47, s51, 0
	v_lshl_add_u64 v[204:205], s[0:1], 0, v[180:181]
	s_add_i32 m0, s56, 0xc000
	ds_read_b128 v[160:163], v207
	ds_read_b128 v[164:167], v207 offset:1024
	ds_read_b128 v[168:171], v207 offset:2048
	ds_read_b128 v[184:187], v207 offset:3072
	ds_read_b128 v[188:191], v207 offset:4096
	ds_read_b128 v[192:195], v207 offset:5120
	ds_read_b128 v[196:199], v207 offset:6144
	ds_read_b128 v[200:203], v207 offset:7168
	global_load_lds_dwordx4 v[204:205], off
	v_lshl_add_u64 v[204:205], s[0:1], 0, v[182:183]
	s_add_i32 m0, s56, 0xe000
	s_nop 0
	global_load_lds_dwordx4 v[204:205], off
	s_waitcnt vmcnt(8)
	s_waitcnt lgkmcnt(0)
	s_setprio 1
	s_barrier
	v_mfma_f32_16x16x32_bf16 v[140:143], v[72:75], v[160:163], v[140:143]
	v_mfma_f32_16x16x32_bf16 v[136:139], v[84:87], v[160:163], v[136:139]
	v_mfma_f32_16x16x32_bf16 v[124:127], v[72:75], v[168:171], v[124:127]
	v_mfma_f32_16x16x32_bf16 v[120:123], v[84:87], v[168:171], v[120:123]
	v_mfma_f32_16x16x32_bf16 v[108:111], v[72:75], v[188:191], v[108:111]
	v_mfma_f32_16x16x32_bf16 v[104:107], v[84:87], v[188:191], v[104:107]
	v_mfma_f32_16x16x32_bf16 v[88:91], v[72:75], v[196:199], v[88:91]
	v_mfma_f32_16x16x32_bf16 v[80:83], v[84:87], v[196:199], v[80:83]
	v_mfma_f32_16x16x32_bf16 v[140:143], v[76:79], v[164:167], v[140:143]
	v_mfma_f32_16x16x32_bf16 v[136:139], v[92:95], v[164:167], v[136:139]
	v_mfma_f32_16x16x32_bf16 v[124:127], v[76:79], v[184:187], v[124:127]
	v_mfma_f32_16x16x32_bf16 v[120:123], v[92:95], v[184:187], v[120:123]
	v_mfma_f32_16x16x32_bf16 v[108:111], v[76:79], v[192:195], v[108:111]
	v_mfma_f32_16x16x32_bf16 v[104:107], v[92:95], v[192:195], v[104:107]
	v_mfma_f32_16x16x32_bf16 v[88:91], v[76:79], v[200:203], v[88:91]
	v_mfma_f32_16x16x32_bf16 v[80:83], v[92:95], v[200:203], v[80:83]
	v_mfma_f32_16x16x32_bf16 v[132:135], v[144:147], v[160:163], v[132:135]
	v_mfma_f32_16x16x32_bf16 v[128:131], v[152:155], v[160:163], v[128:131]
	v_mfma_f32_16x16x32_bf16 v[116:119], v[144:147], v[168:171], v[116:119]
	v_mfma_f32_16x16x32_bf16 v[112:115], v[152:155], v[168:171], v[112:115]
	v_mfma_f32_16x16x32_bf16 v[100:103], v[144:147], v[188:191], v[100:103]
	v_mfma_f32_16x16x32_bf16 v[96:99], v[152:155], v[188:191], v[96:99]
	v_mfma_f32_16x16x32_bf16 v[68:71], v[144:147], v[196:199], v[68:71]
	v_mfma_f32_16x16x32_bf16 v[64:67], v[152:155], v[196:199], v[64:67]
	v_mfma_f32_16x16x32_bf16 v[132:135], v[148:151], v[164:167], v[132:135]
	v_mfma_f32_16x16x32_bf16 v[128:131], v[156:159], v[164:167], v[128:131]
	v_mfma_f32_16x16x32_bf16 v[116:119], v[148:151], v[184:187], v[116:119]
	v_mfma_f32_16x16x32_bf16 v[112:115], v[156:159], v[184:187], v[112:115]
	v_mfma_f32_16x16x32_bf16 v[100:103], v[148:151], v[192:195], v[100:103]
	v_mfma_f32_16x16x32_bf16 v[96:99], v[156:159], v[192:195], v[96:99]
	v_mfma_f32_16x16x32_bf16 v[68:71], v[148:151], v[200:203], v[68:71]
	v_mfma_f32_16x16x32_bf16 v[64:67], v[156:159], v[200:203], v[64:67]
	s_barrier
	s_setprio 0
	s_mov_b32 m0, s31
	v_lshl_add_u64 v[204:205], s[48:49], 0, v[174:175]
	s_add_u32 s0, s48, 0x4000
	ds_read_b128 v[160:163], v207 offset:16384
	ds_read_b128 v[164:167], v207 offset:17408
	ds_read_b128 v[168:171], v207 offset:18432
	ds_read_b128 v[184:187], v207 offset:19456
	ds_read_b128 v[188:191], v207 offset:20480
	ds_read_b128 v[192:195], v207 offset:21504
	ds_read_b128 v[196:199], v207 offset:22528
	ds_read_b128 v[200:203], v207 offset:23552
	global_load_lds_dwordx4 v[204:205], off
	v_lshl_add_u64 v[204:205], s[48:49], 0, v[178:179]
	s_mov_b32 m0, s43
	s_addc_u32 s1, s49, 0
	global_load_lds_dwordx4 v[204:205], off
	v_lshl_add_u64 v[204:205], s[0:1], 0, v[174:175]
	s_mov_b32 m0, s53
	s_nop 0
	global_load_lds_dwordx4 v[204:205], off
	v_lshl_add_u64 v[204:205], s[0:1], 0, v[178:179]
	s_mov_b32 m0, s54
	s_nop 0
	global_load_lds_dwordx4 v[204:205], off
	v_lshl_add_u64 v[204:205], s[50:51], 0, v[172:173]
	s_mov_b32 m0, s56
	s_nop 0
	global_load_lds_dwordx4 v[204:205], off
	v_lshl_add_u64 v[204:205], s[50:51], 0, v[176:177]
	s_mov_b32 m0, s57
	s_nop 0
	global_load_lds_dwordx4 v[204:205], off
	s_waitcnt vmcnt(8)
	s_waitcnt lgkmcnt(0)
	s_setprio 1
	s_barrier
	v_mfma_f32_16x16x32_bf16 v[60:63], v[72:75], v[160:163], v[60:63]
	v_mfma_f32_16x16x32_bf16 v[56:59], v[84:87], v[160:163], v[56:59]
	v_mfma_f32_16x16x32_bf16 v[44:47], v[72:75], v[168:171], v[44:47]
	v_mfma_f32_16x16x32_bf16 v[40:43], v[84:87], v[168:171], v[40:43]
	v_mfma_f32_16x16x32_bf16 v[28:31], v[72:75], v[188:191], v[28:31]
	v_mfma_f32_16x16x32_bf16 v[24:27], v[84:87], v[188:191], v[24:27]
	v_mfma_f32_16x16x32_bf16 v[12:15], v[72:75], v[196:199], v[12:15]
	v_mfma_f32_16x16x32_bf16 v[8:11], v[84:87], v[196:199], v[8:11]
	v_mfma_f32_16x16x32_bf16 v[60:63], v[76:79], v[164:167], v[60:63]
	v_mfma_f32_16x16x32_bf16 v[56:59], v[92:95], v[164:167], v[56:59]
	v_mfma_f32_16x16x32_bf16 v[44:47], v[76:79], v[184:187], v[44:47]
	v_mfma_f32_16x16x32_bf16 v[40:43], v[92:95], v[184:187], v[40:43]
	v_mfma_f32_16x16x32_bf16 v[28:31], v[76:79], v[192:195], v[28:31]
	v_mfma_f32_16x16x32_bf16 v[24:27], v[92:95], v[192:195], v[24:27]
	v_mfma_f32_16x16x32_bf16 v[12:15], v[76:79], v[200:203], v[12:15]
	v_mfma_f32_16x16x32_bf16 v[8:11], v[92:95], v[200:203], v[8:11]
	v_mfma_f32_16x16x32_bf16 v[52:55], v[144:147], v[160:163], v[52:55]
	v_mfma_f32_16x16x32_bf16 v[48:51], v[152:155], v[160:163], v[48:51]
	v_mfma_f32_16x16x32_bf16 v[36:39], v[144:147], v[168:171], v[36:39]
	v_mfma_f32_16x16x32_bf16 v[32:35], v[152:155], v[168:171], v[32:35]
	v_mfma_f32_16x16x32_bf16 v[20:23], v[144:147], v[188:191], v[20:23]
	v_mfma_f32_16x16x32_bf16 v[16:19], v[152:155], v[188:191], v[16:19]
	v_mfma_f32_16x16x32_bf16 v[4:7], v[144:147], v[196:199], v[4:7]
	v_mfma_f32_16x16x32_bf16 v[0:3], v[152:155], v[196:199], v[0:3]
	v_mfma_f32_16x16x32_bf16 v[52:55], v[148:151], v[164:167], v[52:55]
	v_mfma_f32_16x16x32_bf16 v[48:51], v[156:159], v[164:167], v[48:51]
	v_mfma_f32_16x16x32_bf16 v[36:39], v[148:151], v[184:187], v[36:39]
	v_mfma_f32_16x16x32_bf16 v[32:35], v[156:159], v[184:187], v[32:35]
	v_mfma_f32_16x16x32_bf16 v[20:23], v[148:151], v[192:195], v[20:23]
	v_mfma_f32_16x16x32_bf16 v[16:19], v[156:159], v[192:195], v[16:19]
	v_mfma_f32_16x16x32_bf16 v[4:7], v[148:151], v[200:203], v[4:7]
	v_mfma_f32_16x16x32_bf16 v[0:3], v[156:159], v[200:203], v[0:3]
	s_barrier
	s_setprio 0
	v_add_u32_e32 v92, s64, v206
	v_add_u32_e32 v156, s69, v206
	ds_read_b128 v[72:75], v92
	ds_read_b128 v[76:79], v92 offset:1024
	ds_read_b128 v[84:87], v92 offset:2048
	ds_read_b128 v[92:95], v92 offset:3072
	ds_read_b128 v[144:147], v156
	ds_read_b128 v[148:151], v156 offset:1024
	ds_read_b128 v[152:155], v156 offset:2048
	ds_read_b128 v[156:159], v156 offset:3072
	s_add_u32 s0, s50, 0x4000
	s_addc_u32 s1, s51, 0
	s_mov_b32 m0, s58
	v_lshl_add_u64 v[204:205], s[0:1], 0, v[172:173]
	ds_read_b128 v[160:163], v207 offset:32768
	ds_read_b128 v[164:167], v207 offset:33792
	ds_read_b128 v[168:171], v207 offset:34816
	ds_read_b128 v[184:187], v207 offset:35840
	ds_read_b128 v[188:191], v207 offset:36864
	ds_read_b128 v[192:195], v207 offset:37888
	ds_read_b128 v[196:199], v207 offset:38912
	ds_read_b128 v[200:203], v207 offset:39936
	global_load_lds_dwordx4 v[204:205], off
	v_lshl_add_u64 v[204:205], s[0:1], 0, v[176:177]
	s_mov_b32 m0, s59
	s_nop 0
	global_load_lds_dwordx4 v[204:205], off
	s_waitcnt vmcnt(8)
	s_waitcnt lgkmcnt(0)
	s_setprio 1
	s_barrier
	v_mfma_f32_16x16x32_bf16 v[140:143], v[72:75], v[160:163], v[140:143]
	v_mfma_f32_16x16x32_bf16 v[136:139], v[84:87], v[160:163], v[136:139]
	v_mfma_f32_16x16x32_bf16 v[124:127], v[72:75], v[168:171], v[124:127]
	v_mfma_f32_16x16x32_bf16 v[120:123], v[84:87], v[168:171], v[120:123]
	v_mfma_f32_16x16x32_bf16 v[108:111], v[72:75], v[188:191], v[108:111]
	v_mfma_f32_16x16x32_bf16 v[104:107], v[84:87], v[188:191], v[104:107]
	v_mfma_f32_16x16x32_bf16 v[88:91], v[72:75], v[196:199], v[88:91]
	v_mfma_f32_16x16x32_bf16 v[80:83], v[84:87], v[196:199], v[80:83]
	v_mfma_f32_16x16x32_bf16 v[140:143], v[76:79], v[164:167], v[140:143]
	v_mfma_f32_16x16x32_bf16 v[136:139], v[92:95], v[164:167], v[136:139]
	v_mfma_f32_16x16x32_bf16 v[124:127], v[76:79], v[184:187], v[124:127]
	v_mfma_f32_16x16x32_bf16 v[120:123], v[92:95], v[184:187], v[120:123]
	v_mfma_f32_16x16x32_bf16 v[108:111], v[76:79], v[192:195], v[108:111]
	v_mfma_f32_16x16x32_bf16 v[104:107], v[92:95], v[192:195], v[104:107]
	v_mfma_f32_16x16x32_bf16 v[88:91], v[76:79], v[200:203], v[88:91]
	v_mfma_f32_16x16x32_bf16 v[80:83], v[92:95], v[200:203], v[80:83]
	v_mfma_f32_16x16x32_bf16 v[132:135], v[144:147], v[160:163], v[132:135]
	v_mfma_f32_16x16x32_bf16 v[128:131], v[152:155], v[160:163], v[128:131]
	v_mfma_f32_16x16x32_bf16 v[116:119], v[144:147], v[168:171], v[116:119]
	v_mfma_f32_16x16x32_bf16 v[112:115], v[152:155], v[168:171], v[112:115]
	v_mfma_f32_16x16x32_bf16 v[100:103], v[144:147], v[188:191], v[100:103]
	v_mfma_f32_16x16x32_bf16 v[96:99], v[152:155], v[188:191], v[96:99]
	v_mfma_f32_16x16x32_bf16 v[68:71], v[144:147], v[196:199], v[68:71]
	v_mfma_f32_16x16x32_bf16 v[64:67], v[152:155], v[196:199], v[64:67]
	v_mfma_f32_16x16x32_bf16 v[132:135], v[148:151], v[164:167], v[132:135]
	v_mfma_f32_16x16x32_bf16 v[128:131], v[156:159], v[164:167], v[128:131]
	v_mfma_f32_16x16x32_bf16 v[116:119], v[148:151], v[184:187], v[116:119]
	v_mfma_f32_16x16x32_bf16 v[112:115], v[156:159], v[184:187], v[112:115]
	v_mfma_f32_16x16x32_bf16 v[100:103], v[148:151], v[192:195], v[100:103]
	v_mfma_f32_16x16x32_bf16 v[96:99], v[156:159], v[192:195], v[96:99]
	v_mfma_f32_16x16x32_bf16 v[68:71], v[148:151], v[200:203], v[68:71]
	v_mfma_f32_16x16x32_bf16 v[64:67], v[156:159], v[200:203], v[64:67]
	s_barrier
	s_setprio 0
	s_add_u32 s0, s48, 0x8000
	s_addc_u32 s1, s49, 0
	s_mov_b32 m0, s65
	v_lshl_add_u64 v[204:205], s[0:1], 0, v[174:175]
	ds_read_b128 v[160:163], v207 offset:49152
	ds_read_b128 v[164:167], v207 offset:50176
	ds_read_b128 v[168:171], v207 offset:51200
	ds_read_b128 v[184:187], v207 offset:52224
	ds_read_b128 v[188:191], v207 offset:53248
	ds_read_b128 v[192:195], v207 offset:54272
	ds_read_b128 v[196:199], v207 offset:55296
	ds_read_b128 v[200:203], v207 offset:56320
	global_load_lds_dwordx4 v[204:205], off
	v_lshl_add_u64 v[204:205], s[0:1], 0, v[178:179]
	s_add_u32 s0, s48, 0xc000
	s_mov_b32 m0, s66
	s_addc_u32 s1, s49, 0
	global_load_lds_dwordx4 v[204:205], off
	v_lshl_add_u64 v[204:205], s[0:1], 0, v[174:175]
	s_mov_b32 m0, s70
	s_nop 0
	global_load_lds_dwordx4 v[204:205], off
	v_lshl_add_u64 v[204:205], s[0:1], 0, v[178:179]
	s_mov_b32 m0, s71
	s_nop 0
	global_load_lds_dwordx4 v[204:205], off
	v_lshl_add_u64 v[204:205], s[46:47], 0, v[172:173]
	s_mov_b32 m0, s67
	s_nop 0
	global_load_lds_dwordx4 v[204:205], off
	v_lshl_add_u64 v[204:205], s[46:47], 0, v[176:177]
	s_mov_b32 m0, s68
	s_nop 0
	global_load_lds_dwordx4 v[204:205], off
	s_waitcnt vmcnt(8)
	s_waitcnt lgkmcnt(0)
	s_setprio 1
	s_barrier
	v_mfma_f32_16x16x32_bf16 v[60:63], v[72:75], v[160:163], v[60:63]
	v_mfma_f32_16x16x32_bf16 v[56:59], v[84:87], v[160:163], v[56:59]
	v_mfma_f32_16x16x32_bf16 v[44:47], v[72:75], v[168:171], v[44:47]
	v_mfma_f32_16x16x32_bf16 v[40:43], v[84:87], v[168:171], v[40:43]
	v_mfma_f32_16x16x32_bf16 v[28:31], v[72:75], v[188:191], v[28:31]
	v_mfma_f32_16x16x32_bf16 v[24:27], v[84:87], v[188:191], v[24:27]
	v_mfma_f32_16x16x32_bf16 v[12:15], v[72:75], v[196:199], v[12:15]
	v_mfma_f32_16x16x32_bf16 v[8:11], v[84:87], v[196:199], v[8:11]
	v_mfma_f32_16x16x32_bf16 v[60:63], v[76:79], v[164:167], v[60:63]
	v_mfma_f32_16x16x32_bf16 v[56:59], v[92:95], v[164:167], v[56:59]
	v_mfma_f32_16x16x32_bf16 v[44:47], v[76:79], v[184:187], v[44:47]
	v_mfma_f32_16x16x32_bf16 v[40:43], v[92:95], v[184:187], v[40:43]
	v_mfma_f32_16x16x32_bf16 v[28:31], v[76:79], v[192:195], v[28:31]
	v_mfma_f32_16x16x32_bf16 v[24:27], v[92:95], v[192:195], v[24:27]
	v_mfma_f32_16x16x32_bf16 v[12:15], v[76:79], v[200:203], v[12:15]
	v_mfma_f32_16x16x32_bf16 v[8:11], v[92:95], v[200:203], v[8:11]
	v_mfma_f32_16x16x32_bf16 v[52:55], v[144:147], v[160:163], v[52:55]
	v_mfma_f32_16x16x32_bf16 v[48:51], v[152:155], v[160:163], v[48:51]
	v_mfma_f32_16x16x32_bf16 v[36:39], v[144:147], v[168:171], v[36:39]
	v_mfma_f32_16x16x32_bf16 v[32:35], v[152:155], v[168:171], v[32:35]
	v_mfma_f32_16x16x32_bf16 v[20:23], v[144:147], v[188:191], v[20:23]
	v_mfma_f32_16x16x32_bf16 v[16:19], v[152:155], v[188:191], v[16:19]
	v_mfma_f32_16x16x32_bf16 v[4:7], v[144:147], v[196:199], v[4:7]
	v_mfma_f32_16x16x32_bf16 v[0:3], v[152:155], v[196:199], v[0:3]
	v_mfma_f32_16x16x32_bf16 v[52:55], v[148:151], v[164:167], v[52:55]
	v_mfma_f32_16x16x32_bf16 v[48:51], v[156:159], v[164:167], v[48:51]
	v_mfma_f32_16x16x32_bf16 v[36:39], v[148:151], v[184:187], v[36:39]
	v_mfma_f32_16x16x32_bf16 v[32:35], v[156:159], v[184:187], v[32:35]
	v_mfma_f32_16x16x32_bf16 v[20:23], v[148:151], v[192:195], v[20:23]
	v_mfma_f32_16x16x32_bf16 v[16:19], v[156:159], v[192:195], v[16:19]
	v_mfma_f32_16x16x32_bf16 v[4:7], v[148:151], v[200:203], v[4:7]
	v_mfma_f32_16x16x32_bf16 v[0:3], v[156:159], v[200:203], v[0:3]
	s_barrier
	s_setprio 0
	s_add_i32 s76, s76, 2
	s_add_u32 s74, s74, 0x10000
	s_addc_u32 s75, s75, 0
	s_cmpk_gt_u32 s76, 0x7d
	s_mov_b64 s[0:1], s[44:45]
	s_cbranch_scc0 .LBB0_1248
	s_and_b64 vcc, exec, s[22:23]
	s_cbranch_vccz .LBB0_1251
	s_barrier
